# P8 router: each wave covers half its K quarter for both token halves (two accumulators, router matrix read once per workgroup), partner partials exchanged through LDS
# baseline (speedup 1.0000x reference)
; __device__ __forceinline__ float bf_lo(unsigned w) { return __uint_as_float(w << 16); }
; __device__ __forceinline__ float bf_hi(unsigned w) { return __uint_as_float(w & 0xffff0000u); }
; __global__ void __launch_bounds__(512, 2) fwd_kernel(Params p) {
;     ...
;             const int tt = wave & 1, kq = wave >> 1, j = lane & 31, hh = lane >> 5;
;             if (tid < 32) hist[tid] = 0;
;             {
;                 const bf16_t* xr = X1 + (size_t)(blk * 64 + tt * 32 + j) * DM + kq * 512 + hh * 4;
;                 const float* wr_ = WrT + (size_t)j * DM + kq * 512 + hh * 4;
;                 f32x16 acc = {}; float ss = 0.f;
;                 u32x2 xb[2][8]; f32x4 wb[2][8];
; #pragma unroll
;                 for (int i = 0; i < 8; ++i) { xb[0][i] = *(const u32x2*)(xr + i * 8); wb[0][i] = *(const f32x4*)(wr_ + i * 8); }
; #pragma unroll
;                 for (int ch = 0; ch < 8; ++ch) {
;                     if (ch + 1 < 8) {
; #pragma unroll
;                         for (int i = 0; i < 8; ++i) { xb[(ch + 1) & 1][i] = *(const u32x2*)(xr + (ch + 1) * 64 + i * 8); wb[(ch + 1) & 1][i] = *(const f32x4*)(wr_ + (ch + 1) * 64 + i * 8); } }
; #pragma unroll
;                     for (int i = 0; i < 8; ++i) { const u32x2 xp = xb[ch & 1][i]; const f32x4 xv = {bf_lo(xp.x), bf_hi(xp.x), bf_lo(xp.y), bf_hi(xp.y)}, wv = wb[ch & 1][i];
;                         acc = __builtin_amdgcn_mfma_f32_32x32x2f32(wv.x, xv.x, acc, 0, 0, 0); acc = __builtin_amdgcn_mfma_f32_32x32x2f32(wv.y, xv.y, acc, 0, 0, 0);
;                         acc = __builtin_amdgcn_mfma_f32_32x32x2f32(wv.z, xv.z, acc, 0, 0, 0); acc = __builtin_amdgcn_mfma_f32_32x32x2f32(wv.w, xv.w, acc, 0, 0, 0);
;                         ss += (xv.x * xv.x + xv.y * xv.y) + (xv.z * xv.z + xv.w * xv.w); }
;                 }
.LBB0_982:
	s_and_saveexec_b64 s[10:11], s[4:5]
	ds_write_b32 v132, v87 offset:53760
	s_or_b64 exec, exec, s[10:11]
	s_lshl_b32 s10, s78, 6
	v_or_b32_e32 v0, s10, v133
	v_ashrrev_i32_e32 v1, 31, v0
	v_lshlrev_b64 v[0:1], 12, v[0:1]
	v_lshl_add_u64 v[98:99], v[88:89], 0, v[0:1]
	v_mbcnt_lo_u32_b32 v81, -1, 0
	v_mbcnt_hi_u32_b32 v81, -1, v81
	v_lshrrev_b32_e32 v81, 5, v81
	v_bfe_u32 v104, v133, 5, 1
	v_mov_b32_e32 v83, 0
	v_lshlrev_b32_e32 v82, 3, v81
	v_lshl_or_b32 v82, v104, 9, v82
	v_lshl_add_u64 v[100:101], v[98:99], 0, v[82:83]
	v_lshlrev_b32_e32 v82, 4, v81
	v_lshl_or_b32 v82, v104, 10, v82
	v_lshl_add_u64 v[102:103], v[90:91], 0, v[82:83]
	v_cmp_eq_u32_e64 s[46:47], 1, v104
	v_mov_b32_e32 v124, 0x20000
	v_mov_b32_e32 v125, 0xfffe0000
	v_mov_b32_e32 v126, -1
	v_cndmask_b32_e64 v124, v124, v125, s[46:47]
	v_cndmask_b32_e64 v125, v83, v126, s[46:47]
	v_lshl_add_u64 v[106:107], v[100:101], 0, v[124:125]
	v_mov_b32_e32 v80, 0
	v_mov_b32_e32 v128, 0
	global_load_dwordx4 v[148:151], v[100:101], off
	global_load_dwordx4 v[152:155], v[106:107], off
	global_load_dwordx4 v[156:159], v[102:103], off
	global_load_dwordx4 v[160:163], v[102:103], off offset:16
	global_load_dwordx4 v[164:167], v[100:101], off offset:32
	global_load_dwordx4 v[168:171], v[106:107], off offset:32
	global_load_dwordx4 v[172:175], v[102:103], off offset:64
	global_load_dwordx4 v[176:179], v[102:103], off offset:80
	global_load_dwordx4 v[180:183], v[100:101], off offset:64
	global_load_dwordx4 v[184:187], v[106:107], off offset:64
	global_load_dwordx4 v[188:191], v[102:103], off offset:128
	global_load_dwordx4 v[192:195], v[102:103], off offset:144
	global_load_dwordx4 v[196:199], v[100:101], off offset:96
	global_load_dwordx4 v[200:203], v[106:107], off offset:96
	global_load_dwordx4 v[204:207], v[102:103], off offset:192
	global_load_dwordx4 v[208:211], v[102:103], off offset:208
	global_load_dwordx4 v[16:19], v[100:101], off offset:128
	global_load_dwordx4 v[20:23], v[106:107], off offset:128
	global_load_dwordx4 v[24:27], v[102:103], off offset:256
	global_load_dwordx4 v[28:31], v[102:103], off offset:272
	global_load_dwordx4 v[32:35], v[100:101], off offset:160
	global_load_dwordx4 v[36:39], v[106:107], off offset:160
	global_load_dwordx4 v[40:43], v[102:103], off offset:320
	global_load_dwordx4 v[44:47], v[102:103], off offset:336
	global_load_dwordx4 v[48:51], v[100:101], off offset:192
	global_load_dwordx4 v[52:55], v[106:107], off offset:192
	global_load_dwordx4 v[56:59], v[102:103], off offset:384
	global_load_dwordx4 v[60:63], v[102:103], off offset:400
	global_load_dwordx4 v[64:67], v[100:101], off offset:224
	global_load_dwordx4 v[68:71], v[106:107], off offset:224
	global_load_dwordx4 v[72:75], v[102:103], off offset:448
	global_load_dwordx4 v[76:79], v[102:103], off offset:464
	s_waitcnt vmcnt(28)
	v_lshlrev_b32_e32 v212, 16, v148
	v_lshlrev_b32_e32 v220, 16, v152
	v_and_b32_e32 v213, 0xffff0000, v148
	v_and_b32_e32 v221, 0xffff0000, v152
	v_lshlrev_b32_e32 v214, 16, v149
	v_lshlrev_b32_e32 v222, 16, v153
	v_and_b32_e32 v215, 0xffff0000, v149
	v_and_b32_e32 v223, 0xffff0000, v153
	v_lshlrev_b32_e32 v216, 16, v150
	v_lshlrev_b32_e32 v224, 16, v154
	v_and_b32_e32 v217, 0xffff0000, v150
	v_and_b32_e32 v225, 0xffff0000, v154
	v_lshlrev_b32_e32 v218, 16, v151
	v_lshlrev_b32_e32 v226, 16, v155
	v_and_b32_e32 v219, 0xffff0000, v151
	v_and_b32_e32 v227, 0xffff0000, v155
	s_waitcnt vmcnt(24)
	v_mfma_f32_32x32x2_f32 v[0:15], v156, v212, 0
	v_lshlrev_b32_e32 v228, 16, v164
	v_fmac_f32_e32 v80, v212, v212
	v_mfma_f32_32x32x2_f32 v[108:123], v156, v220, 0
	v_lshlrev_b32_e32 v236, 16, v168
	v_fmac_f32_e32 v128, v220, v220
	v_mfma_f32_32x32x2_f32 v[0:15], v157, v213, v[0:15]
	v_and_b32_e32 v229, 0xffff0000, v164
	v_fmac_f32_e32 v80, v213, v213
	v_mfma_f32_32x32x2_f32 v[108:123], v157, v221, v[108:123]
	v_and_b32_e32 v237, 0xffff0000, v168
	v_fmac_f32_e32 v128, v221, v221
	v_mfma_f32_32x32x2_f32 v[0:15], v158, v214, v[0:15]
	v_lshlrev_b32_e32 v230, 16, v165
	v_fmac_f32_e32 v80, v214, v214
	v_mfma_f32_32x32x2_f32 v[108:123], v158, v222, v[108:123]
	v_lshlrev_b32_e32 v238, 16, v169
	v_fmac_f32_e32 v128, v222, v222
	v_mfma_f32_32x32x2_f32 v[0:15], v159, v215, v[0:15]
	v_and_b32_e32 v231, 0xffff0000, v165
	v_fmac_f32_e32 v80, v215, v215
	v_mfma_f32_32x32x2_f32 v[108:123], v159, v223, v[108:123]
	v_and_b32_e32 v239, 0xffff0000, v169
	v_fmac_f32_e32 v128, v223, v223
	v_mfma_f32_32x32x2_f32 v[0:15], v160, v216, v[0:15]
	v_lshlrev_b32_e32 v232, 16, v166
	v_fmac_f32_e32 v80, v216, v216
	v_mfma_f32_32x32x2_f32 v[108:123], v160, v224, v[108:123]
	v_lshlrev_b32_e32 v240, 16, v170
	v_fmac_f32_e32 v128, v224, v224
	v_mfma_f32_32x32x2_f32 v[0:15], v161, v217, v[0:15]
	v_and_b32_e32 v233, 0xffff0000, v166
	v_fmac_f32_e32 v80, v217, v217
	v_mfma_f32_32x32x2_f32 v[108:123], v161, v225, v[108:123]
	v_and_b32_e32 v241, 0xffff0000, v170
	v_fmac_f32_e32 v128, v225, v225
	v_mfma_f32_32x32x2_f32 v[0:15], v162, v218, v[0:15]
	v_lshlrev_b32_e32 v234, 16, v167
	v_fmac_f32_e32 v80, v218, v218
	v_mfma_f32_32x32x2_f32 v[108:123], v162, v226, v[108:123]
	v_lshlrev_b32_e32 v242, 16, v171
	v_fmac_f32_e32 v128, v226, v226
	v_mfma_f32_32x32x2_f32 v[0:15], v163, v219, v[0:15]
	v_and_b32_e32 v235, 0xffff0000, v167
	v_fmac_f32_e32 v80, v219, v219
	v_mfma_f32_32x32x2_f32 v[108:123], v163, v227, v[108:123]
	v_and_b32_e32 v243, 0xffff0000, v171
	v_fmac_f32_e32 v128, v227, v227
	s_waitcnt vmcnt(20)
; __device__ __forceinline__ float bf_lo(unsigned w) { return __uint_as_float(w << 16); }
; __device__ __forceinline__ float bf_hi(unsigned w) { return __uint_as_float(w & 0xffff0000u); }
; __global__ void __launch_bounds__(512, 2) fwd_kernel(Params p) {
;     ...
; #pragma unroll
;                 for (int ch = 0; ch < 8; ++ch) {
;                     if (ch + 1 < 8) {
; #pragma unroll
;                         for (int i = 0; i < 8; ++i) { xb[(ch + 1) & 1][i] = *(const u32x2*)(xr + (ch + 1) * 64 + i * 8); wb[(ch + 1) & 1][i] = *(const f32x4*)(wr_ + (ch + 1) * 64 + i * 8); } }
; #pragma unroll
;                     for (int i = 0; i < 8; ++i) { const u32x2 xp = xb[ch & 1][i]; const f32x4 xv = {bf_lo(xp.x), bf_hi(xp.x), bf_lo(xp.y), bf_hi(xp.y)}, wv = wb[ch & 1][i];
;                         acc = __builtin_amdgcn_mfma_f32_32x32x2f32(wv.x, xv.x, acc, 0, 0, 0); acc = __builtin_amdgcn_mfma_f32_32x32x2f32(wv.y, xv.y, acc, 0, 0, 0);
;                         acc = __builtin_amdgcn_mfma_f32_32x32x2f32(wv.z, xv.z, acc, 0, 0, 0); acc = __builtin_amdgcn_mfma_f32_32x32x2f32(wv.w, xv.w, acc, 0, 0, 0);
;                         ss += (xv.x * xv.x + xv.y * xv.y) + (xv.z * xv.z + xv.w * xv.w); }
;                 }
	v_mfma_f32_32x32x2_f32 v[0:15], v172, v228, v[0:15]
	v_lshlrev_b32_e32 v212, 16, v180
	v_fmac_f32_e32 v80, v228, v228
	v_mfma_f32_32x32x2_f32 v[108:123], v172, v236, v[108:123]
	v_lshlrev_b32_e32 v220, 16, v184
	v_fmac_f32_e32 v128, v236, v236
	v_mfma_f32_32x32x2_f32 v[0:15], v173, v229, v[0:15]
	v_and_b32_e32 v213, 0xffff0000, v180
	v_fmac_f32_e32 v80, v229, v229
	v_mfma_f32_32x32x2_f32 v[108:123], v173, v237, v[108:123]
	v_and_b32_e32 v221, 0xffff0000, v184
	v_fmac_f32_e32 v128, v237, v237
	v_mfma_f32_32x32x2_f32 v[0:15], v174, v230, v[0:15]
	v_lshlrev_b32_e32 v214, 16, v181
	v_fmac_f32_e32 v80, v230, v230
	v_mfma_f32_32x32x2_f32 v[108:123], v174, v238, v[108:123]
	v_lshlrev_b32_e32 v222, 16, v185
	v_fmac_f32_e32 v128, v238, v238
	v_mfma_f32_32x32x2_f32 v[0:15], v175, v231, v[0:15]
	v_and_b32_e32 v215, 0xffff0000, v181
	v_fmac_f32_e32 v80, v231, v231
	v_mfma_f32_32x32x2_f32 v[108:123], v175, v239, v[108:123]
	v_and_b32_e32 v223, 0xffff0000, v185
	v_fmac_f32_e32 v128, v239, v239
	v_mfma_f32_32x32x2_f32 v[0:15], v176, v232, v[0:15]
	v_lshlrev_b32_e32 v216, 16, v182
	v_fmac_f32_e32 v80, v232, v232
	v_mfma_f32_32x32x2_f32 v[108:123], v176, v240, v[108:123]
	v_lshlrev_b32_e32 v224, 16, v186
	v_fmac_f32_e32 v128, v240, v240
	v_mfma_f32_32x32x2_f32 v[0:15], v177, v233, v[0:15]
	v_and_b32_e32 v217, 0xffff0000, v182
	v_fmac_f32_e32 v80, v233, v233
	v_mfma_f32_32x32x2_f32 v[108:123], v177, v241, v[108:123]
	v_and_b32_e32 v225, 0xffff0000, v186
	v_fmac_f32_e32 v128, v241, v241
	v_mfma_f32_32x32x2_f32 v[0:15], v178, v234, v[0:15]
	v_lshlrev_b32_e32 v218, 16, v183
	v_fmac_f32_e32 v80, v234, v234
	v_mfma_f32_32x32x2_f32 v[108:123], v178, v242, v[108:123]
	v_lshlrev_b32_e32 v226, 16, v187
	v_fmac_f32_e32 v128, v242, v242
	v_mfma_f32_32x32x2_f32 v[0:15], v179, v235, v[0:15]
	v_and_b32_e32 v219, 0xffff0000, v183
	v_fmac_f32_e32 v80, v235, v235
	v_mfma_f32_32x32x2_f32 v[108:123], v179, v243, v[108:123]
	v_and_b32_e32 v227, 0xffff0000, v187
	v_fmac_f32_e32 v128, v243, v243
	s_waitcnt vmcnt(16)
	v_mfma_f32_32x32x2_f32 v[0:15], v188, v212, v[0:15]
	v_lshlrev_b32_e32 v228, 16, v196
	v_fmac_f32_e32 v80, v212, v212
	v_mfma_f32_32x32x2_f32 v[108:123], v188, v220, v[108:123]
	v_lshlrev_b32_e32 v236, 16, v200
	v_fmac_f32_e32 v128, v220, v220
	v_mfma_f32_32x32x2_f32 v[0:15], v189, v213, v[0:15]
	v_and_b32_e32 v229, 0xffff0000, v196
	v_fmac_f32_e32 v80, v213, v213
	v_mfma_f32_32x32x2_f32 v[108:123], v189, v221, v[108:123]
	v_and_b32_e32 v237, 0xffff0000, v200
	v_fmac_f32_e32 v128, v221, v221
	v_mfma_f32_32x32x2_f32 v[0:15], v190, v214, v[0:15]
	v_lshlrev_b32_e32 v230, 16, v197
	v_fmac_f32_e32 v80, v214, v214
	v_mfma_f32_32x32x2_f32 v[108:123], v190, v222, v[108:123]
	v_lshlrev_b32_e32 v238, 16, v201
	v_fmac_f32_e32 v128, v222, v222
	v_mfma_f32_32x32x2_f32 v[0:15], v191, v215, v[0:15]
	v_and_b32_e32 v231, 0xffff0000, v197
	v_fmac_f32_e32 v80, v215, v215
	v_mfma_f32_32x32x2_f32 v[108:123], v191, v223, v[108:123]
	v_and_b32_e32 v239, 0xffff0000, v201
	v_fmac_f32_e32 v128, v223, v223
	v_mfma_f32_32x32x2_f32 v[0:15], v192, v216, v[0:15]
	v_lshlrev_b32_e32 v232, 16, v198
	v_fmac_f32_e32 v80, v216, v216
	v_mfma_f32_32x32x2_f32 v[108:123], v192, v224, v[108:123]
	v_lshlrev_b32_e32 v240, 16, v202
	v_fmac_f32_e32 v128, v224, v224
	v_mfma_f32_32x32x2_f32 v[0:15], v193, v217, v[0:15]
	v_and_b32_e32 v233, 0xffff0000, v198
	v_fmac_f32_e32 v80, v217, v217
	v_mfma_f32_32x32x2_f32 v[108:123], v193, v225, v[108:123]
	v_and_b32_e32 v241, 0xffff0000, v202
	v_fmac_f32_e32 v128, v225, v225
	v_mfma_f32_32x32x2_f32 v[0:15], v194, v218, v[0:15]
	v_lshlrev_b32_e32 v234, 16, v199
	v_fmac_f32_e32 v80, v218, v218
	v_mfma_f32_32x32x2_f32 v[108:123], v194, v226, v[108:123]
	v_lshlrev_b32_e32 v242, 16, v203
	v_fmac_f32_e32 v128, v226, v226
	v_mfma_f32_32x32x2_f32 v[0:15], v195, v219, v[0:15]
	v_and_b32_e32 v235, 0xffff0000, v199
	v_fmac_f32_e32 v80, v219, v219
	v_mfma_f32_32x32x2_f32 v[108:123], v195, v227, v[108:123]
	v_and_b32_e32 v243, 0xffff0000, v203
	v_fmac_f32_e32 v128, v227, v227
	s_waitcnt vmcnt(12)
	v_mfma_f32_32x32x2_f32 v[0:15], v204, v228, v[0:15]
	v_lshlrev_b32_e32 v212, 16, v16
	v_fmac_f32_e32 v80, v228, v228
	v_mfma_f32_32x32x2_f32 v[108:123], v204, v236, v[108:123]
	v_lshlrev_b32_e32 v220, 16, v20
	v_fmac_f32_e32 v128, v236, v236
	v_mfma_f32_32x32x2_f32 v[0:15], v205, v229, v[0:15]
	v_and_b32_e32 v213, 0xffff0000, v16
	v_fmac_f32_e32 v80, v229, v229
	v_mfma_f32_32x32x2_f32 v[108:123], v205, v237, v[108:123]
	v_and_b32_e32 v221, 0xffff0000, v20
	v_fmac_f32_e32 v128, v237, v237
	v_mfma_f32_32x32x2_f32 v[0:15], v206, v230, v[0:15]
	v_lshlrev_b32_e32 v214, 16, v17
	v_fmac_f32_e32 v80, v230, v230
	v_mfma_f32_32x32x2_f32 v[108:123], v206, v238, v[108:123]
	v_lshlrev_b32_e32 v222, 16, v21
	v_fmac_f32_e32 v128, v238, v238
	v_mfma_f32_32x32x2_f32 v[0:15], v207, v231, v[0:15]
	v_and_b32_e32 v215, 0xffff0000, v17
	v_fmac_f32_e32 v80, v231, v231
	v_mfma_f32_32x32x2_f32 v[108:123], v207, v239, v[108:123]
	v_and_b32_e32 v223, 0xffff0000, v21
	v_fmac_f32_e32 v128, v239, v239
	v_mfma_f32_32x32x2_f32 v[0:15], v208, v232, v[0:15]
	v_lshlrev_b32_e32 v216, 16, v18
	v_fmac_f32_e32 v80, v232, v232
	v_mfma_f32_32x32x2_f32 v[108:123], v208, v240, v[108:123]
	v_lshlrev_b32_e32 v224, 16, v22
	v_fmac_f32_e32 v128, v240, v240
	v_mfma_f32_32x32x2_f32 v[0:15], v209, v233, v[0:15]
	v_and_b32_e32 v217, 0xffff0000, v18
	v_fmac_f32_e32 v80, v233, v233
	v_mfma_f32_32x32x2_f32 v[108:123], v209, v241, v[108:123]
	v_and_b32_e32 v225, 0xffff0000, v22
	v_fmac_f32_e32 v128, v241, v241
	v_mfma_f32_32x32x2_f32 v[0:15], v210, v234, v[0:15]
	v_lshlrev_b32_e32 v218, 16, v19
	v_fmac_f32_e32 v80, v234, v234
	v_mfma_f32_32x32x2_f32 v[108:123], v210, v242, v[108:123]
	v_lshlrev_b32_e32 v226, 16, v23
	v_fmac_f32_e32 v128, v242, v242
	v_mfma_f32_32x32x2_f32 v[0:15], v211, v235, v[0:15]
	v_and_b32_e32 v219, 0xffff0000, v19
	v_fmac_f32_e32 v80, v235, v235
	v_mfma_f32_32x32x2_f32 v[108:123], v211, v243, v[108:123]
	v_and_b32_e32 v227, 0xffff0000, v23
	v_fmac_f32_e32 v128, v243, v243
	global_load_dwordx4 v[148:151], v[100:101], off offset:256
	global_load_dwordx4 v[152:155], v[106:107], off offset:256
	global_load_dwordx4 v[156:159], v[102:103], off offset:512
	global_load_dwordx4 v[160:163], v[102:103], off offset:528
	global_load_dwordx4 v[164:167], v[100:101], off offset:288
	global_load_dwordx4 v[168:171], v[106:107], off offset:288
	global_load_dwordx4 v[172:175], v[102:103], off offset:576
	global_load_dwordx4 v[176:179], v[102:103], off offset:592
	global_load_dwordx4 v[180:183], v[100:101], off offset:320
	global_load_dwordx4 v[184:187], v[106:107], off offset:320
	global_load_dwordx4 v[188:191], v[102:103], off offset:640
	global_load_dwordx4 v[192:195], v[102:103], off offset:656
	global_load_dwordx4 v[196:199], v[100:101], off offset:352
	global_load_dwordx4 v[200:203], v[106:107], off offset:352
	global_load_dwordx4 v[204:207], v[102:103], off offset:704
	global_load_dwordx4 v[208:211], v[102:103], off offset:720
	s_waitcnt vmcnt(24)
; __device__ __forceinline__ float bf_lo(unsigned w) { return __uint_as_float(w << 16); }
; __device__ __forceinline__ float bf_hi(unsigned w) { return __uint_as_float(w & 0xffff0000u); }
; __global__ void __launch_bounds__(512, 2) fwd_kernel(Params p) {
;     ...
; #pragma unroll
;                 for (int ch = 0; ch < 8; ++ch) {
;                     if (ch + 1 < 8) {
; #pragma unroll
;                         for (int i = 0; i < 8; ++i) { xb[(ch + 1) & 1][i] = *(const u32x2*)(xr + (ch + 1) * 64 + i * 8); wb[(ch + 1) & 1][i] = *(const f32x4*)(wr_ + (ch + 1) * 64 + i * 8); } }
; #pragma unroll
;                     for (int i = 0; i < 8; ++i) { const u32x2 xp = xb[ch & 1][i]; const f32x4 xv = {bf_lo(xp.x), bf_hi(xp.x), bf_lo(xp.y), bf_hi(xp.y)}, wv = wb[ch & 1][i];
;                         acc = __builtin_amdgcn_mfma_f32_32x32x2f32(wv.x, xv.x, acc, 0, 0, 0); acc = __builtin_amdgcn_mfma_f32_32x32x2f32(wv.y, xv.y, acc, 0, 0, 0);
;                         acc = __builtin_amdgcn_mfma_f32_32x32x2f32(wv.z, xv.z, acc, 0, 0, 0); acc = __builtin_amdgcn_mfma_f32_32x32x2f32(wv.w, xv.w, acc, 0, 0, 0);
;                         ss += (xv.x * xv.x + xv.y * xv.y) + (xv.z * xv.z + xv.w * xv.w); }
;                 }
	v_mfma_f32_32x32x2_f32 v[0:15], v24, v212, v[0:15]
	v_lshlrev_b32_e32 v228, 16, v32
	v_fmac_f32_e32 v80, v212, v212
	v_mfma_f32_32x32x2_f32 v[108:123], v24, v220, v[108:123]
	v_lshlrev_b32_e32 v236, 16, v36
	v_fmac_f32_e32 v128, v220, v220
	v_mfma_f32_32x32x2_f32 v[0:15], v25, v213, v[0:15]
	v_and_b32_e32 v229, 0xffff0000, v32
	v_fmac_f32_e32 v80, v213, v213
	v_mfma_f32_32x32x2_f32 v[108:123], v25, v221, v[108:123]
	v_and_b32_e32 v237, 0xffff0000, v36
	v_fmac_f32_e32 v128, v221, v221
	v_mfma_f32_32x32x2_f32 v[0:15], v26, v214, v[0:15]
	v_lshlrev_b32_e32 v230, 16, v33
	v_fmac_f32_e32 v80, v214, v214
	v_mfma_f32_32x32x2_f32 v[108:123], v26, v222, v[108:123]
	v_lshlrev_b32_e32 v238, 16, v37
	v_fmac_f32_e32 v128, v222, v222
	v_mfma_f32_32x32x2_f32 v[0:15], v27, v215, v[0:15]
	v_and_b32_e32 v231, 0xffff0000, v33
	v_fmac_f32_e32 v80, v215, v215
	v_mfma_f32_32x32x2_f32 v[108:123], v27, v223, v[108:123]
	v_and_b32_e32 v239, 0xffff0000, v37
	v_fmac_f32_e32 v128, v223, v223
	v_mfma_f32_32x32x2_f32 v[0:15], v28, v216, v[0:15]
	v_lshlrev_b32_e32 v232, 16, v34
	v_fmac_f32_e32 v80, v216, v216
	v_mfma_f32_32x32x2_f32 v[108:123], v28, v224, v[108:123]
	v_lshlrev_b32_e32 v240, 16, v38
	v_fmac_f32_e32 v128, v224, v224
	v_mfma_f32_32x32x2_f32 v[0:15], v29, v217, v[0:15]
	v_and_b32_e32 v233, 0xffff0000, v34
	v_fmac_f32_e32 v80, v217, v217
	v_mfma_f32_32x32x2_f32 v[108:123], v29, v225, v[108:123]
	v_and_b32_e32 v241, 0xffff0000, v38
	v_fmac_f32_e32 v128, v225, v225
	v_mfma_f32_32x32x2_f32 v[0:15], v30, v218, v[0:15]
	v_lshlrev_b32_e32 v234, 16, v35
	v_fmac_f32_e32 v80, v218, v218
	v_mfma_f32_32x32x2_f32 v[108:123], v30, v226, v[108:123]
	v_lshlrev_b32_e32 v242, 16, v39
	v_fmac_f32_e32 v128, v226, v226
	v_mfma_f32_32x32x2_f32 v[0:15], v31, v219, v[0:15]
	v_and_b32_e32 v235, 0xffff0000, v35
	v_fmac_f32_e32 v80, v219, v219
	v_mfma_f32_32x32x2_f32 v[108:123], v31, v227, v[108:123]
	v_and_b32_e32 v243, 0xffff0000, v39
	v_fmac_f32_e32 v128, v227, v227
	s_waitcnt vmcnt(20)
	v_mfma_f32_32x32x2_f32 v[0:15], v40, v228, v[0:15]
	v_lshlrev_b32_e32 v212, 16, v48
	v_fmac_f32_e32 v80, v228, v228
	v_mfma_f32_32x32x2_f32 v[108:123], v40, v236, v[108:123]
	v_lshlrev_b32_e32 v220, 16, v52
	v_fmac_f32_e32 v128, v236, v236
	v_mfma_f32_32x32x2_f32 v[0:15], v41, v229, v[0:15]
	v_and_b32_e32 v213, 0xffff0000, v48
	v_fmac_f32_e32 v80, v229, v229
	v_mfma_f32_32x32x2_f32 v[108:123], v41, v237, v[108:123]
	v_and_b32_e32 v221, 0xffff0000, v52
	v_fmac_f32_e32 v128, v237, v237
	v_mfma_f32_32x32x2_f32 v[0:15], v42, v230, v[0:15]
	v_lshlrev_b32_e32 v214, 16, v49
	v_fmac_f32_e32 v80, v230, v230
	v_mfma_f32_32x32x2_f32 v[108:123], v42, v238, v[108:123]
	v_lshlrev_b32_e32 v222, 16, v53
	v_fmac_f32_e32 v128, v238, v238
	v_mfma_f32_32x32x2_f32 v[0:15], v43, v231, v[0:15]
	v_and_b32_e32 v215, 0xffff0000, v49
	v_fmac_f32_e32 v80, v231, v231
	v_mfma_f32_32x32x2_f32 v[108:123], v43, v239, v[108:123]
	v_and_b32_e32 v223, 0xffff0000, v53
	v_fmac_f32_e32 v128, v239, v239
	v_mfma_f32_32x32x2_f32 v[0:15], v44, v232, v[0:15]
	v_lshlrev_b32_e32 v216, 16, v50
	v_fmac_f32_e32 v80, v232, v232
	v_mfma_f32_32x32x2_f32 v[108:123], v44, v240, v[108:123]
	v_lshlrev_b32_e32 v224, 16, v54
	v_fmac_f32_e32 v128, v240, v240
	v_mfma_f32_32x32x2_f32 v[0:15], v45, v233, v[0:15]
	v_and_b32_e32 v217, 0xffff0000, v50
	v_fmac_f32_e32 v80, v233, v233
	v_mfma_f32_32x32x2_f32 v[108:123], v45, v241, v[108:123]
	v_and_b32_e32 v225, 0xffff0000, v54
	v_fmac_f32_e32 v128, v241, v241
	v_mfma_f32_32x32x2_f32 v[0:15], v46, v234, v[0:15]
	v_lshlrev_b32_e32 v218, 16, v51
	v_fmac_f32_e32 v80, v234, v234
	v_mfma_f32_32x32x2_f32 v[108:123], v46, v242, v[108:123]
	v_lshlrev_b32_e32 v226, 16, v55
	v_fmac_f32_e32 v128, v242, v242
	v_mfma_f32_32x32x2_f32 v[0:15], v47, v235, v[0:15]
	v_and_b32_e32 v219, 0xffff0000, v51
	v_fmac_f32_e32 v80, v235, v235
	v_mfma_f32_32x32x2_f32 v[108:123], v47, v243, v[108:123]
	v_and_b32_e32 v227, 0xffff0000, v55
	v_fmac_f32_e32 v128, v243, v243
	s_waitcnt vmcnt(16)
	v_mfma_f32_32x32x2_f32 v[0:15], v56, v212, v[0:15]
	v_lshlrev_b32_e32 v228, 16, v64
	v_fmac_f32_e32 v80, v212, v212
	v_mfma_f32_32x32x2_f32 v[108:123], v56, v220, v[108:123]
	v_lshlrev_b32_e32 v236, 16, v68
	v_fmac_f32_e32 v128, v220, v220
	v_mfma_f32_32x32x2_f32 v[0:15], v57, v213, v[0:15]
	v_and_b32_e32 v229, 0xffff0000, v64
	v_fmac_f32_e32 v80, v213, v213
	v_mfma_f32_32x32x2_f32 v[108:123], v57, v221, v[108:123]
	v_and_b32_e32 v237, 0xffff0000, v68
	v_fmac_f32_e32 v128, v221, v221
	v_mfma_f32_32x32x2_f32 v[0:15], v58, v214, v[0:15]
	v_lshlrev_b32_e32 v230, 16, v65
	v_fmac_f32_e32 v80, v214, v214
	v_mfma_f32_32x32x2_f32 v[108:123], v58, v222, v[108:123]
	v_lshlrev_b32_e32 v238, 16, v69
	v_fmac_f32_e32 v128, v222, v222
	v_mfma_f32_32x32x2_f32 v[0:15], v59, v215, v[0:15]
	v_and_b32_e32 v231, 0xffff0000, v65
	v_fmac_f32_e32 v80, v215, v215
	v_mfma_f32_32x32x2_f32 v[108:123], v59, v223, v[108:123]
	v_and_b32_e32 v239, 0xffff0000, v69
	v_fmac_f32_e32 v128, v223, v223
	v_mfma_f32_32x32x2_f32 v[0:15], v60, v216, v[0:15]
	v_lshlrev_b32_e32 v232, 16, v66
	v_fmac_f32_e32 v80, v216, v216
	v_mfma_f32_32x32x2_f32 v[108:123], v60, v224, v[108:123]
	v_lshlrev_b32_e32 v240, 16, v70
	v_fmac_f32_e32 v128, v224, v224
	v_mfma_f32_32x32x2_f32 v[0:15], v61, v217, v[0:15]
	v_and_b32_e32 v233, 0xffff0000, v66
	v_fmac_f32_e32 v80, v217, v217
	v_mfma_f32_32x32x2_f32 v[108:123], v61, v225, v[108:123]
	v_and_b32_e32 v241, 0xffff0000, v70
	v_fmac_f32_e32 v128, v225, v225
	v_mfma_f32_32x32x2_f32 v[0:15], v62, v218, v[0:15]
	v_lshlrev_b32_e32 v234, 16, v67
	v_fmac_f32_e32 v80, v218, v218
	v_mfma_f32_32x32x2_f32 v[108:123], v62, v226, v[108:123]
	v_lshlrev_b32_e32 v242, 16, v71
	v_fmac_f32_e32 v128, v226, v226
	v_mfma_f32_32x32x2_f32 v[0:15], v63, v219, v[0:15]
	v_and_b32_e32 v235, 0xffff0000, v67
	v_fmac_f32_e32 v80, v219, v219
	v_mfma_f32_32x32x2_f32 v[108:123], v63, v227, v[108:123]
	v_and_b32_e32 v243, 0xffff0000, v71
	v_fmac_f32_e32 v128, v227, v227
	s_waitcnt vmcnt(12)
; __device__ __forceinline__ float bf_lo(unsigned w) { return __uint_as_float(w << 16); }
; __device__ __forceinline__ float bf_hi(unsigned w) { return __uint_as_float(w & 0xffff0000u); }
; __global__ void __launch_bounds__(512, 2) fwd_kernel(Params p) {
;     ...
; #pragma unroll
;                 for (int ch = 0; ch < 8; ++ch) {
;                     if (ch + 1 < 8) {
; #pragma unroll
;                         for (int i = 0; i < 8; ++i) { xb[(ch + 1) & 1][i] = *(const u32x2*)(xr + (ch + 1) * 64 + i * 8); wb[(ch + 1) & 1][i] = *(const f32x4*)(wr_ + (ch + 1) * 64 + i * 8); } }
; #pragma unroll
;                     for (int i = 0; i < 8; ++i) { const u32x2 xp = xb[ch & 1][i]; const f32x4 xv = {bf_lo(xp.x), bf_hi(xp.x), bf_lo(xp.y), bf_hi(xp.y)}, wv = wb[ch & 1][i];
;                         acc = __builtin_amdgcn_mfma_f32_32x32x2f32(wv.x, xv.x, acc, 0, 0, 0); acc = __builtin_amdgcn_mfma_f32_32x32x2f32(wv.y, xv.y, acc, 0, 0, 0);
;                         acc = __builtin_amdgcn_mfma_f32_32x32x2f32(wv.z, xv.z, acc, 0, 0, 0); acc = __builtin_amdgcn_mfma_f32_32x32x2f32(wv.w, xv.w, acc, 0, 0, 0);
;                         ss += (xv.x * xv.x + xv.y * xv.y) + (xv.z * xv.z + xv.w * xv.w); }
;                 }
	v_mfma_f32_32x32x2_f32 v[0:15], v72, v228, v[0:15]
	v_lshlrev_b32_e32 v212, 16, v148
	v_fmac_f32_e32 v80, v228, v228
	v_mfma_f32_32x32x2_f32 v[108:123], v72, v236, v[108:123]
	v_lshlrev_b32_e32 v220, 16, v152
	v_fmac_f32_e32 v128, v236, v236
	v_mfma_f32_32x32x2_f32 v[0:15], v73, v229, v[0:15]
	v_and_b32_e32 v213, 0xffff0000, v148
	v_fmac_f32_e32 v80, v229, v229
	v_mfma_f32_32x32x2_f32 v[108:123], v73, v237, v[108:123]
	v_and_b32_e32 v221, 0xffff0000, v152
	v_fmac_f32_e32 v128, v237, v237
	v_mfma_f32_32x32x2_f32 v[0:15], v74, v230, v[0:15]
	v_lshlrev_b32_e32 v214, 16, v149
	v_fmac_f32_e32 v80, v230, v230
	v_mfma_f32_32x32x2_f32 v[108:123], v74, v238, v[108:123]
	v_lshlrev_b32_e32 v222, 16, v153
	v_fmac_f32_e32 v128, v238, v238
	v_mfma_f32_32x32x2_f32 v[0:15], v75, v231, v[0:15]
	v_and_b32_e32 v215, 0xffff0000, v149
	v_fmac_f32_e32 v80, v231, v231
	v_mfma_f32_32x32x2_f32 v[108:123], v75, v239, v[108:123]
	v_and_b32_e32 v223, 0xffff0000, v153
	v_fmac_f32_e32 v128, v239, v239
	v_mfma_f32_32x32x2_f32 v[0:15], v76, v232, v[0:15]
	v_lshlrev_b32_e32 v216, 16, v150
	v_fmac_f32_e32 v80, v232, v232
	v_mfma_f32_32x32x2_f32 v[108:123], v76, v240, v[108:123]
	v_lshlrev_b32_e32 v224, 16, v154
	v_fmac_f32_e32 v128, v240, v240
	v_mfma_f32_32x32x2_f32 v[0:15], v77, v233, v[0:15]
	v_and_b32_e32 v217, 0xffff0000, v150
	v_fmac_f32_e32 v80, v233, v233
	v_mfma_f32_32x32x2_f32 v[108:123], v77, v241, v[108:123]
	v_and_b32_e32 v225, 0xffff0000, v154
	v_fmac_f32_e32 v128, v241, v241
	v_mfma_f32_32x32x2_f32 v[0:15], v78, v234, v[0:15]
	v_lshlrev_b32_e32 v218, 16, v151
	v_fmac_f32_e32 v80, v234, v234
	v_mfma_f32_32x32x2_f32 v[108:123], v78, v242, v[108:123]
	v_lshlrev_b32_e32 v226, 16, v155
	v_fmac_f32_e32 v128, v242, v242
	v_mfma_f32_32x32x2_f32 v[0:15], v79, v235, v[0:15]
	v_and_b32_e32 v219, 0xffff0000, v151
	v_fmac_f32_e32 v80, v235, v235
	v_mfma_f32_32x32x2_f32 v[108:123], v79, v243, v[108:123]
	v_and_b32_e32 v227, 0xffff0000, v155
	v_fmac_f32_e32 v128, v243, v243
	global_load_dwordx4 v[16:19], v[100:101], off offset:384
	global_load_dwordx4 v[20:23], v[106:107], off offset:384
	global_load_dwordx4 v[24:27], v[102:103], off offset:768
	global_load_dwordx4 v[28:31], v[102:103], off offset:784
	global_load_dwordx4 v[32:35], v[100:101], off offset:416
	global_load_dwordx4 v[36:39], v[106:107], off offset:416
	global_load_dwordx4 v[40:43], v[102:103], off offset:832
	global_load_dwordx4 v[44:47], v[102:103], off offset:848
	global_load_dwordx4 v[48:51], v[100:101], off offset:448
	global_load_dwordx4 v[52:55], v[106:107], off offset:448
	global_load_dwordx4 v[56:59], v[102:103], off offset:896
	global_load_dwordx4 v[60:63], v[102:103], off offset:912
	global_load_dwordx4 v[64:67], v[100:101], off offset:480
	global_load_dwordx4 v[68:71], v[106:107], off offset:480
	global_load_dwordx4 v[72:75], v[102:103], off offset:960
	global_load_dwordx4 v[76:79], v[102:103], off offset:976
	s_waitcnt vmcnt(24)
	v_mfma_f32_32x32x2_f32 v[0:15], v156, v212, v[0:15]
	v_lshlrev_b32_e32 v228, 16, v164
	v_fmac_f32_e32 v80, v212, v212
	v_mfma_f32_32x32x2_f32 v[108:123], v156, v220, v[108:123]
	v_lshlrev_b32_e32 v236, 16, v168
	v_fmac_f32_e32 v128, v220, v220
	v_mfma_f32_32x32x2_f32 v[0:15], v157, v213, v[0:15]
	v_and_b32_e32 v229, 0xffff0000, v164
	v_fmac_f32_e32 v80, v213, v213
	v_mfma_f32_32x32x2_f32 v[108:123], v157, v221, v[108:123]
	v_and_b32_e32 v237, 0xffff0000, v168
	v_fmac_f32_e32 v128, v221, v221
	v_mfma_f32_32x32x2_f32 v[0:15], v158, v214, v[0:15]
	v_lshlrev_b32_e32 v230, 16, v165
	v_fmac_f32_e32 v80, v214, v214
	v_mfma_f32_32x32x2_f32 v[108:123], v158, v222, v[108:123]
	v_lshlrev_b32_e32 v238, 16, v169
	v_fmac_f32_e32 v128, v222, v222
	v_mfma_f32_32x32x2_f32 v[0:15], v159, v215, v[0:15]
	v_and_b32_e32 v231, 0xffff0000, v165
	v_fmac_f32_e32 v80, v215, v215
	v_mfma_f32_32x32x2_f32 v[108:123], v159, v223, v[108:123]
	v_and_b32_e32 v239, 0xffff0000, v169
	v_fmac_f32_e32 v128, v223, v223
	v_mfma_f32_32x32x2_f32 v[0:15], v160, v216, v[0:15]
	v_lshlrev_b32_e32 v232, 16, v166
	v_fmac_f32_e32 v80, v216, v216
	v_mfma_f32_32x32x2_f32 v[108:123], v160, v224, v[108:123]
	v_lshlrev_b32_e32 v240, 16, v170
	v_fmac_f32_e32 v128, v224, v224
	v_mfma_f32_32x32x2_f32 v[0:15], v161, v217, v[0:15]
	v_and_b32_e32 v233, 0xffff0000, v166
	v_fmac_f32_e32 v80, v217, v217
	v_mfma_f32_32x32x2_f32 v[108:123], v161, v225, v[108:123]
	v_and_b32_e32 v241, 0xffff0000, v170
	v_fmac_f32_e32 v128, v225, v225
	v_mfma_f32_32x32x2_f32 v[0:15], v162, v218, v[0:15]
	v_lshlrev_b32_e32 v234, 16, v167
	v_fmac_f32_e32 v80, v218, v218
	v_mfma_f32_32x32x2_f32 v[108:123], v162, v226, v[108:123]
	v_lshlrev_b32_e32 v242, 16, v171
	v_fmac_f32_e32 v128, v226, v226
	v_mfma_f32_32x32x2_f32 v[0:15], v163, v219, v[0:15]
	v_and_b32_e32 v235, 0xffff0000, v167
	v_fmac_f32_e32 v80, v219, v219
	v_mfma_f32_32x32x2_f32 v[108:123], v163, v227, v[108:123]
	v_and_b32_e32 v243, 0xffff0000, v171
	v_fmac_f32_e32 v128, v227, v227
	s_waitcnt vmcnt(20)
; __device__ __forceinline__ float bf_lo(unsigned w) { return __uint_as_float(w << 16); }
; __device__ __forceinline__ float bf_hi(unsigned w) { return __uint_as_float(w & 0xffff0000u); }
; __global__ void __launch_bounds__(512, 2) fwd_kernel(Params p) {
;     ...
; #pragma unroll
;                 for (int ch = 0; ch < 8; ++ch) {
;                     if (ch + 1 < 8) {
; #pragma unroll
;                         for (int i = 0; i < 8; ++i) { xb[(ch + 1) & 1][i] = *(const u32x2*)(xr + (ch + 1) * 64 + i * 8); wb[(ch + 1) & 1][i] = *(const f32x4*)(wr_ + (ch + 1) * 64 + i * 8); } }
; #pragma unroll
;                     for (int i = 0; i < 8; ++i) { const u32x2 xp = xb[ch & 1][i]; const f32x4 xv = {bf_lo(xp.x), bf_hi(xp.x), bf_lo(xp.y), bf_hi(xp.y)}, wv = wb[ch & 1][i];
;                         acc = __builtin_amdgcn_mfma_f32_32x32x2f32(wv.x, xv.x, acc, 0, 0, 0); acc = __builtin_amdgcn_mfma_f32_32x32x2f32(wv.y, xv.y, acc, 0, 0, 0);
;                         acc = __builtin_amdgcn_mfma_f32_32x32x2f32(wv.z, xv.z, acc, 0, 0, 0); acc = __builtin_amdgcn_mfma_f32_32x32x2f32(wv.w, xv.w, acc, 0, 0, 0);
;                         ss += (xv.x * xv.x + xv.y * xv.y) + (xv.z * xv.z + xv.w * xv.w); }
;                 }
	v_mfma_f32_32x32x2_f32 v[0:15], v172, v228, v[0:15]
	v_lshlrev_b32_e32 v212, 16, v180
	v_fmac_f32_e32 v80, v228, v228
	v_mfma_f32_32x32x2_f32 v[108:123], v172, v236, v[108:123]
	v_lshlrev_b32_e32 v220, 16, v184
	v_fmac_f32_e32 v128, v236, v236
	v_mfma_f32_32x32x2_f32 v[0:15], v173, v229, v[0:15]
	v_and_b32_e32 v213, 0xffff0000, v180
	v_fmac_f32_e32 v80, v229, v229
	v_mfma_f32_32x32x2_f32 v[108:123], v173, v237, v[108:123]
	v_and_b32_e32 v221, 0xffff0000, v184
	v_fmac_f32_e32 v128, v237, v237
	v_mfma_f32_32x32x2_f32 v[0:15], v174, v230, v[0:15]
	v_lshlrev_b32_e32 v214, 16, v181
	v_fmac_f32_e32 v80, v230, v230
	v_mfma_f32_32x32x2_f32 v[108:123], v174, v238, v[108:123]
	v_lshlrev_b32_e32 v222, 16, v185
	v_fmac_f32_e32 v128, v238, v238
	v_mfma_f32_32x32x2_f32 v[0:15], v175, v231, v[0:15]
	v_and_b32_e32 v215, 0xffff0000, v181
	v_fmac_f32_e32 v80, v231, v231
	v_mfma_f32_32x32x2_f32 v[108:123], v175, v239, v[108:123]
	v_and_b32_e32 v223, 0xffff0000, v185
	v_fmac_f32_e32 v128, v239, v239
	v_mfma_f32_32x32x2_f32 v[0:15], v176, v232, v[0:15]
	v_lshlrev_b32_e32 v216, 16, v182
	v_fmac_f32_e32 v80, v232, v232
	v_mfma_f32_32x32x2_f32 v[108:123], v176, v240, v[108:123]
	v_lshlrev_b32_e32 v224, 16, v186
	v_fmac_f32_e32 v128, v240, v240
	v_mfma_f32_32x32x2_f32 v[0:15], v177, v233, v[0:15]
	v_and_b32_e32 v217, 0xffff0000, v182
	v_fmac_f32_e32 v80, v233, v233
	v_mfma_f32_32x32x2_f32 v[108:123], v177, v241, v[108:123]
	v_and_b32_e32 v225, 0xffff0000, v186
	v_fmac_f32_e32 v128, v241, v241
	v_mfma_f32_32x32x2_f32 v[0:15], v178, v234, v[0:15]
	v_lshlrev_b32_e32 v218, 16, v183
	v_fmac_f32_e32 v80, v234, v234
	v_mfma_f32_32x32x2_f32 v[108:123], v178, v242, v[108:123]
	v_lshlrev_b32_e32 v226, 16, v187
	v_fmac_f32_e32 v128, v242, v242
	v_mfma_f32_32x32x2_f32 v[0:15], v179, v235, v[0:15]
	v_and_b32_e32 v219, 0xffff0000, v183
	v_fmac_f32_e32 v80, v235, v235
	v_mfma_f32_32x32x2_f32 v[108:123], v179, v243, v[108:123]
	v_and_b32_e32 v227, 0xffff0000, v187
	v_fmac_f32_e32 v128, v243, v243
	s_waitcnt vmcnt(16)
	v_mfma_f32_32x32x2_f32 v[0:15], v188, v212, v[0:15]
	v_lshlrev_b32_e32 v228, 16, v196
	v_fmac_f32_e32 v80, v212, v212
	v_mfma_f32_32x32x2_f32 v[108:123], v188, v220, v[108:123]
	v_lshlrev_b32_e32 v236, 16, v200
	v_fmac_f32_e32 v128, v220, v220
	v_mfma_f32_32x32x2_f32 v[0:15], v189, v213, v[0:15]
	v_and_b32_e32 v229, 0xffff0000, v196
	v_fmac_f32_e32 v80, v213, v213
	v_mfma_f32_32x32x2_f32 v[108:123], v189, v221, v[108:123]
	v_and_b32_e32 v237, 0xffff0000, v200
	v_fmac_f32_e32 v128, v221, v221
	v_mfma_f32_32x32x2_f32 v[0:15], v190, v214, v[0:15]
	v_lshlrev_b32_e32 v230, 16, v197
	v_fmac_f32_e32 v80, v214, v214
	v_mfma_f32_32x32x2_f32 v[108:123], v190, v222, v[108:123]
	v_lshlrev_b32_e32 v238, 16, v201
	v_fmac_f32_e32 v128, v222, v222
	v_mfma_f32_32x32x2_f32 v[0:15], v191, v215, v[0:15]
	v_and_b32_e32 v231, 0xffff0000, v197
	v_fmac_f32_e32 v80, v215, v215
	v_mfma_f32_32x32x2_f32 v[108:123], v191, v223, v[108:123]
	v_and_b32_e32 v239, 0xffff0000, v201
	v_fmac_f32_e32 v128, v223, v223
	v_mfma_f32_32x32x2_f32 v[0:15], v192, v216, v[0:15]
	v_lshlrev_b32_e32 v232, 16, v198
	v_fmac_f32_e32 v80, v216, v216
	v_mfma_f32_32x32x2_f32 v[108:123], v192, v224, v[108:123]
	v_lshlrev_b32_e32 v240, 16, v202
	v_fmac_f32_e32 v128, v224, v224
	v_mfma_f32_32x32x2_f32 v[0:15], v193, v217, v[0:15]
	v_and_b32_e32 v233, 0xffff0000, v198
	v_fmac_f32_e32 v80, v217, v217
	v_mfma_f32_32x32x2_f32 v[108:123], v193, v225, v[108:123]
	v_and_b32_e32 v241, 0xffff0000, v202
	v_fmac_f32_e32 v128, v225, v225
	v_mfma_f32_32x32x2_f32 v[0:15], v194, v218, v[0:15]
	v_lshlrev_b32_e32 v234, 16, v199
	v_fmac_f32_e32 v80, v218, v218
	v_mfma_f32_32x32x2_f32 v[108:123], v194, v226, v[108:123]
	v_lshlrev_b32_e32 v242, 16, v203
	v_fmac_f32_e32 v128, v226, v226
	v_mfma_f32_32x32x2_f32 v[0:15], v195, v219, v[0:15]
	v_and_b32_e32 v235, 0xffff0000, v199
	v_fmac_f32_e32 v80, v219, v219
	v_mfma_f32_32x32x2_f32 v[108:123], v195, v227, v[108:123]
	v_and_b32_e32 v243, 0xffff0000, v203
	v_fmac_f32_e32 v128, v227, v227
	s_waitcnt vmcnt(12)
	v_mfma_f32_32x32x2_f32 v[0:15], v204, v228, v[0:15]
	v_lshlrev_b32_e32 v212, 16, v16
	v_fmac_f32_e32 v80, v228, v228
	v_mfma_f32_32x32x2_f32 v[108:123], v204, v236, v[108:123]
	v_lshlrev_b32_e32 v220, 16, v20
	v_fmac_f32_e32 v128, v236, v236
	v_mfma_f32_32x32x2_f32 v[0:15], v205, v229, v[0:15]
	v_and_b32_e32 v213, 0xffff0000, v16
	v_fmac_f32_e32 v80, v229, v229
	v_mfma_f32_32x32x2_f32 v[108:123], v205, v237, v[108:123]
	v_and_b32_e32 v221, 0xffff0000, v20
	v_fmac_f32_e32 v128, v237, v237
	v_mfma_f32_32x32x2_f32 v[0:15], v206, v230, v[0:15]
	v_lshlrev_b32_e32 v214, 16, v17
	v_fmac_f32_e32 v80, v230, v230
	v_mfma_f32_32x32x2_f32 v[108:123], v206, v238, v[108:123]
	v_lshlrev_b32_e32 v222, 16, v21
	v_fmac_f32_e32 v128, v238, v238
	v_mfma_f32_32x32x2_f32 v[0:15], v207, v231, v[0:15]
	v_and_b32_e32 v215, 0xffff0000, v17
	v_fmac_f32_e32 v80, v231, v231
	v_mfma_f32_32x32x2_f32 v[108:123], v207, v239, v[108:123]
	v_and_b32_e32 v223, 0xffff0000, v21
	v_fmac_f32_e32 v128, v239, v239
	v_mfma_f32_32x32x2_f32 v[0:15], v208, v232, v[0:15]
	v_lshlrev_b32_e32 v216, 16, v18
	v_fmac_f32_e32 v80, v232, v232
	v_mfma_f32_32x32x2_f32 v[108:123], v208, v240, v[108:123]
	v_lshlrev_b32_e32 v224, 16, v22
	v_fmac_f32_e32 v128, v240, v240
	v_mfma_f32_32x32x2_f32 v[0:15], v209, v233, v[0:15]
	v_and_b32_e32 v217, 0xffff0000, v18
	v_fmac_f32_e32 v80, v233, v233
	v_mfma_f32_32x32x2_f32 v[108:123], v209, v241, v[108:123]
	v_and_b32_e32 v225, 0xffff0000, v22
	v_fmac_f32_e32 v128, v241, v241
	v_mfma_f32_32x32x2_f32 v[0:15], v210, v234, v[0:15]
	v_lshlrev_b32_e32 v218, 16, v19
	v_fmac_f32_e32 v80, v234, v234
	v_mfma_f32_32x32x2_f32 v[108:123], v210, v242, v[108:123]
	v_lshlrev_b32_e32 v226, 16, v23
	v_fmac_f32_e32 v128, v242, v242
	v_mfma_f32_32x32x2_f32 v[0:15], v211, v235, v[0:15]
	v_and_b32_e32 v219, 0xffff0000, v19
	v_fmac_f32_e32 v80, v235, v235
	v_mfma_f32_32x32x2_f32 v[108:123], v211, v243, v[108:123]
	v_and_b32_e32 v227, 0xffff0000, v23
	v_fmac_f32_e32 v128, v243, v243
	s_waitcnt vmcnt(8)
; __device__ __forceinline__ float bf_lo(unsigned w) { return __uint_as_float(w << 16); }
; __device__ __forceinline__ float bf_hi(unsigned w) { return __uint_as_float(w & 0xffff0000u); }
; __global__ void __launch_bounds__(512, 2) fwd_kernel(Params p) {
;     ...
; #pragma unroll
;                 for (int ch = 0; ch < 8; ++ch) {
;                     if (ch + 1 < 8) {
; #pragma unroll
;                         for (int i = 0; i < 8; ++i) { xb[(ch + 1) & 1][i] = *(const u32x2*)(xr + (ch + 1) * 64 + i * 8); wb[(ch + 1) & 1][i] = *(const f32x4*)(wr_ + (ch + 1) * 64 + i * 8); } }
; #pragma unroll
;                     for (int i = 0; i < 8; ++i) { const u32x2 xp = xb[ch & 1][i]; const f32x4 xv = {bf_lo(xp.x), bf_hi(xp.x), bf_lo(xp.y), bf_hi(xp.y)}, wv = wb[ch & 1][i];
;                         acc = __builtin_amdgcn_mfma_f32_32x32x2f32(wv.x, xv.x, acc, 0, 0, 0); acc = __builtin_amdgcn_mfma_f32_32x32x2f32(wv.y, xv.y, acc, 0, 0, 0);
;                         acc = __builtin_amdgcn_mfma_f32_32x32x2f32(wv.z, xv.z, acc, 0, 0, 0); acc = __builtin_amdgcn_mfma_f32_32x32x2f32(wv.w, xv.w, acc, 0, 0, 0);
;                         ss += (xv.x * xv.x + xv.y * xv.y) + (xv.z * xv.z + xv.w * xv.w); }
;                 }
	v_mfma_f32_32x32x2_f32 v[0:15], v24, v212, v[0:15]
	v_lshlrev_b32_e32 v228, 16, v32
	v_fmac_f32_e32 v80, v212, v212
	v_mfma_f32_32x32x2_f32 v[108:123], v24, v220, v[108:123]
	v_lshlrev_b32_e32 v236, 16, v36
	v_fmac_f32_e32 v128, v220, v220
	v_mfma_f32_32x32x2_f32 v[0:15], v25, v213, v[0:15]
	v_and_b32_e32 v229, 0xffff0000, v32
	v_fmac_f32_e32 v80, v213, v213
	v_mfma_f32_32x32x2_f32 v[108:123], v25, v221, v[108:123]
	v_and_b32_e32 v237, 0xffff0000, v36
	v_fmac_f32_e32 v128, v221, v221
	v_mfma_f32_32x32x2_f32 v[0:15], v26, v214, v[0:15]
	v_lshlrev_b32_e32 v230, 16, v33
	v_fmac_f32_e32 v80, v214, v214
	v_mfma_f32_32x32x2_f32 v[108:123], v26, v222, v[108:123]
	v_lshlrev_b32_e32 v238, 16, v37
	v_fmac_f32_e32 v128, v222, v222
	v_mfma_f32_32x32x2_f32 v[0:15], v27, v215, v[0:15]
	v_and_b32_e32 v231, 0xffff0000, v33
	v_fmac_f32_e32 v80, v215, v215
	v_mfma_f32_32x32x2_f32 v[108:123], v27, v223, v[108:123]
	v_and_b32_e32 v239, 0xffff0000, v37
	v_fmac_f32_e32 v128, v223, v223
	v_mfma_f32_32x32x2_f32 v[0:15], v28, v216, v[0:15]
	v_lshlrev_b32_e32 v232, 16, v34
	v_fmac_f32_e32 v80, v216, v216
	v_mfma_f32_32x32x2_f32 v[108:123], v28, v224, v[108:123]
	v_lshlrev_b32_e32 v240, 16, v38
	v_fmac_f32_e32 v128, v224, v224
	v_mfma_f32_32x32x2_f32 v[0:15], v29, v217, v[0:15]
	v_and_b32_e32 v233, 0xffff0000, v34
	v_fmac_f32_e32 v80, v217, v217
	v_mfma_f32_32x32x2_f32 v[108:123], v29, v225, v[108:123]
	v_and_b32_e32 v241, 0xffff0000, v38
	v_fmac_f32_e32 v128, v225, v225
	v_mfma_f32_32x32x2_f32 v[0:15], v30, v218, v[0:15]
	v_lshlrev_b32_e32 v234, 16, v35
	v_fmac_f32_e32 v80, v218, v218
	v_mfma_f32_32x32x2_f32 v[108:123], v30, v226, v[108:123]
	v_lshlrev_b32_e32 v242, 16, v39
	v_fmac_f32_e32 v128, v226, v226
	v_mfma_f32_32x32x2_f32 v[0:15], v31, v219, v[0:15]
	v_and_b32_e32 v235, 0xffff0000, v35
	v_fmac_f32_e32 v80, v219, v219
	v_mfma_f32_32x32x2_f32 v[108:123], v31, v227, v[108:123]
	v_and_b32_e32 v243, 0xffff0000, v39
	v_fmac_f32_e32 v128, v227, v227
	s_waitcnt vmcnt(4)
	v_mfma_f32_32x32x2_f32 v[0:15], v40, v228, v[0:15]
	v_lshlrev_b32_e32 v212, 16, v48
	v_fmac_f32_e32 v80, v228, v228
	v_mfma_f32_32x32x2_f32 v[108:123], v40, v236, v[108:123]
	v_lshlrev_b32_e32 v220, 16, v52
	v_fmac_f32_e32 v128, v236, v236
	v_mfma_f32_32x32x2_f32 v[0:15], v41, v229, v[0:15]
	v_and_b32_e32 v213, 0xffff0000, v48
	v_fmac_f32_e32 v80, v229, v229
	v_mfma_f32_32x32x2_f32 v[108:123], v41, v237, v[108:123]
	v_and_b32_e32 v221, 0xffff0000, v52
	v_fmac_f32_e32 v128, v237, v237
	v_mfma_f32_32x32x2_f32 v[0:15], v42, v230, v[0:15]
	v_lshlrev_b32_e32 v214, 16, v49
	v_fmac_f32_e32 v80, v230, v230
	v_mfma_f32_32x32x2_f32 v[108:123], v42, v238, v[108:123]
	v_lshlrev_b32_e32 v222, 16, v53
	v_fmac_f32_e32 v128, v238, v238
	v_mfma_f32_32x32x2_f32 v[0:15], v43, v231, v[0:15]
	v_and_b32_e32 v215, 0xffff0000, v49
	v_fmac_f32_e32 v80, v231, v231
	v_mfma_f32_32x32x2_f32 v[108:123], v43, v239, v[108:123]
	v_and_b32_e32 v223, 0xffff0000, v53
	v_fmac_f32_e32 v128, v239, v239
	v_mfma_f32_32x32x2_f32 v[0:15], v44, v232, v[0:15]
	v_lshlrev_b32_e32 v216, 16, v50
	v_fmac_f32_e32 v80, v232, v232
	v_mfma_f32_32x32x2_f32 v[108:123], v44, v240, v[108:123]
	v_lshlrev_b32_e32 v224, 16, v54
	v_fmac_f32_e32 v128, v240, v240
	v_mfma_f32_32x32x2_f32 v[0:15], v45, v233, v[0:15]
	v_and_b32_e32 v217, 0xffff0000, v50
	v_fmac_f32_e32 v80, v233, v233
	v_mfma_f32_32x32x2_f32 v[108:123], v45, v241, v[108:123]
	v_and_b32_e32 v225, 0xffff0000, v54
	v_fmac_f32_e32 v128, v241, v241
	v_mfma_f32_32x32x2_f32 v[0:15], v46, v234, v[0:15]
	v_lshlrev_b32_e32 v218, 16, v51
	v_fmac_f32_e32 v80, v234, v234
	v_mfma_f32_32x32x2_f32 v[108:123], v46, v242, v[108:123]
	v_lshlrev_b32_e32 v226, 16, v55
	v_fmac_f32_e32 v128, v242, v242
	v_mfma_f32_32x32x2_f32 v[0:15], v47, v235, v[0:15]
	v_and_b32_e32 v219, 0xffff0000, v51
	v_fmac_f32_e32 v80, v235, v235
	v_mfma_f32_32x32x2_f32 v[108:123], v47, v243, v[108:123]
	v_and_b32_e32 v227, 0xffff0000, v55
	v_fmac_f32_e32 v128, v243, v243
	s_waitcnt vmcnt(0)
	v_mfma_f32_32x32x2_f32 v[0:15], v56, v212, v[0:15]
	v_lshlrev_b32_e32 v228, 16, v64
	v_fmac_f32_e32 v80, v212, v212
	v_mfma_f32_32x32x2_f32 v[108:123], v56, v220, v[108:123]
	v_lshlrev_b32_e32 v236, 16, v68
	v_fmac_f32_e32 v128, v220, v220
	v_mfma_f32_32x32x2_f32 v[0:15], v57, v213, v[0:15]
	v_and_b32_e32 v229, 0xffff0000, v64
	v_fmac_f32_e32 v80, v213, v213
	v_mfma_f32_32x32x2_f32 v[108:123], v57, v221, v[108:123]
	v_and_b32_e32 v237, 0xffff0000, v68
	v_fmac_f32_e32 v128, v221, v221
	v_mfma_f32_32x32x2_f32 v[0:15], v58, v214, v[0:15]
	v_lshlrev_b32_e32 v230, 16, v65
	v_fmac_f32_e32 v80, v214, v214
	v_mfma_f32_32x32x2_f32 v[108:123], v58, v222, v[108:123]
	v_lshlrev_b32_e32 v238, 16, v69
	v_fmac_f32_e32 v128, v222, v222
	v_mfma_f32_32x32x2_f32 v[0:15], v59, v215, v[0:15]
	v_and_b32_e32 v231, 0xffff0000, v65
	v_fmac_f32_e32 v80, v215, v215
	v_mfma_f32_32x32x2_f32 v[108:123], v59, v223, v[108:123]
	v_and_b32_e32 v239, 0xffff0000, v69
	v_fmac_f32_e32 v128, v223, v223
	v_mfma_f32_32x32x2_f32 v[0:15], v60, v216, v[0:15]
	v_lshlrev_b32_e32 v232, 16, v66
	v_fmac_f32_e32 v80, v216, v216
	v_mfma_f32_32x32x2_f32 v[108:123], v60, v224, v[108:123]
	v_lshlrev_b32_e32 v240, 16, v70
	v_fmac_f32_e32 v128, v224, v224
	v_mfma_f32_32x32x2_f32 v[0:15], v61, v217, v[0:15]
	v_and_b32_e32 v233, 0xffff0000, v66
	v_fmac_f32_e32 v80, v217, v217
	v_mfma_f32_32x32x2_f32 v[108:123], v61, v225, v[108:123]
	v_and_b32_e32 v241, 0xffff0000, v70
	v_fmac_f32_e32 v128, v225, v225
	v_mfma_f32_32x32x2_f32 v[0:15], v62, v218, v[0:15]
	v_lshlrev_b32_e32 v234, 16, v67
	v_fmac_f32_e32 v80, v218, v218
	v_mfma_f32_32x32x2_f32 v[108:123], v62, v226, v[108:123]
	v_lshlrev_b32_e32 v242, 16, v71
; #define LAS __attribute__((address_space(3)))
; __device__ __forceinline__ float bf_lo(unsigned w) { return __uint_as_float(w << 16); }
; __device__ __forceinline__ float bf_hi(unsigned w) { return __uint_as_float(w & 0xffff0000u); }
; __global__ void __launch_bounds__(512, 2) fwd_kernel(Params p) {
;     ...
; #pragma unroll
;                     for (int i = 0; i < 8; ++i) { const u32x2 xp = xb[ch & 1][i]; const f32x4 xv = {bf_lo(xp.x), bf_hi(xp.x), bf_lo(xp.y), bf_hi(xp.y)}, wv = wb[ch & 1][i];
;                         acc = __builtin_amdgcn_mfma_f32_32x32x2f32(wv.x, xv.x, acc, 0, 0, 0); acc = __builtin_amdgcn_mfma_f32_32x32x2f32(wv.y, xv.y, acc, 0, 0, 0);
;                         acc = __builtin_amdgcn_mfma_f32_32x32x2f32(wv.z, xv.z, acc, 0, 0, 0); acc = __builtin_amdgcn_mfma_f32_32x32x2f32(wv.w, xv.w, acc, 0, 0, 0);
;                         ss += (xv.x * xv.x + xv.y * xv.y) + (xv.z * xv.z + xv.w * xv.w); }
;                 }
;                 LAS float* pp = part + ((kq * 2 + tt) * 32 + j) * 33;
; #pragma unroll
;                 for (int r = 0; r < 16; ++r) pp[(r & 3) + 8 * (r >> 2) + 4 * hh] = acc[r];
;                 ssq[((kq * 2 + tt) * 32 + j) * 2 + hh] = ss;
	v_fmac_f32_e32 v128, v226, v226
	v_mfma_f32_32x32x2_f32 v[0:15], v63, v219, v[0:15]
	v_and_b32_e32 v235, 0xffff0000, v67
	v_fmac_f32_e32 v80, v219, v219
	v_mfma_f32_32x32x2_f32 v[108:123], v63, v227, v[108:123]
	v_and_b32_e32 v243, 0xffff0000, v71
	v_fmac_f32_e32 v128, v227, v227
	v_mfma_f32_32x32x2_f32 v[0:15], v72, v228, v[0:15]
	v_fmac_f32_e32 v80, v228, v228
	v_mfma_f32_32x32x2_f32 v[108:123], v72, v236, v[108:123]
	v_fmac_f32_e32 v128, v236, v236
	v_mfma_f32_32x32x2_f32 v[0:15], v73, v229, v[0:15]
	v_fmac_f32_e32 v80, v229, v229
	v_mfma_f32_32x32x2_f32 v[108:123], v73, v237, v[108:123]
	v_fmac_f32_e32 v128, v237, v237
	v_mfma_f32_32x32x2_f32 v[0:15], v74, v230, v[0:15]
	v_fmac_f32_e32 v80, v230, v230
	v_mfma_f32_32x32x2_f32 v[108:123], v74, v238, v[108:123]
	v_fmac_f32_e32 v128, v238, v238
	v_mfma_f32_32x32x2_f32 v[0:15], v75, v231, v[0:15]
	v_fmac_f32_e32 v80, v231, v231
	v_mfma_f32_32x32x2_f32 v[108:123], v75, v239, v[108:123]
	v_fmac_f32_e32 v128, v239, v239
	v_mfma_f32_32x32x2_f32 v[0:15], v76, v232, v[0:15]
	v_fmac_f32_e32 v80, v232, v232
	v_mfma_f32_32x32x2_f32 v[108:123], v76, v240, v[108:123]
	v_fmac_f32_e32 v128, v240, v240
	v_mfma_f32_32x32x2_f32 v[0:15], v77, v233, v[0:15]
	v_fmac_f32_e32 v80, v233, v233
	v_mfma_f32_32x32x2_f32 v[108:123], v77, v241, v[108:123]
	v_fmac_f32_e32 v128, v241, v241
	v_mfma_f32_32x32x2_f32 v[0:15], v78, v234, v[0:15]
	v_fmac_f32_e32 v80, v234, v234
	v_mfma_f32_32x32x2_f32 v[108:123], v78, v242, v[108:123]
	v_fmac_f32_e32 v128, v242, v242
	v_mfma_f32_32x32x2_f32 v[0:15], v79, v235, v[0:15]
	v_fmac_f32_e32 v80, v235, v235
	v_mfma_f32_32x32x2_f32 v[108:123], v79, v243, v[108:123]
	v_fmac_f32_e32 v128, v243, v243
	v_lshrrev_b32_e32 v124, 6, v84
	v_and_b32_e32 v125, 63, v84
	v_mul_u32_u24_e32 v126, 0x1200, v124
	v_lshl_add_u32 v126, v125, 2, v126
	v_add_u32_e32 v126, 0x10000, v126
	v_xor_b32_e32 v124, 1, v124
	v_mul_u32_u24_e32 v127, 0x1200, v124
	v_lshl_add_u32 v127, v125, 2, v127
	v_add_u32_e32 v127, 0x10000, v127
	s_nop 15
	ds_write_b32 v126, v108
	ds_write_b32 v126, v109 offset:256
	ds_write_b32 v126, v110 offset:512
	ds_write_b32 v126, v111 offset:768
	ds_write_b32 v126, v112 offset:1024
	ds_write_b32 v126, v113 offset:1280
	ds_write_b32 v126, v114 offset:1536
	ds_write_b32 v126, v115 offset:1792
	ds_write_b32 v126, v116 offset:2048
	ds_write_b32 v126, v117 offset:2304
	ds_write_b32 v126, v118 offset:2560
	ds_write_b32 v126, v119 offset:2816
	ds_write_b32 v126, v120 offset:3072
	ds_write_b32 v126, v121 offset:3328
	ds_write_b32 v126, v122 offset:3584
	ds_write_b32 v126, v123 offset:3840
	ds_write_b32 v126, v128 offset:4096
	s_waitcnt lgkmcnt(0)
	s_barrier
	ds_read_b32 v16, v127
	ds_read_b32 v17, v127 offset:256
	ds_read_b32 v18, v127 offset:512
	ds_read_b32 v19, v127 offset:768
	ds_read_b32 v20, v127 offset:1024
	ds_read_b32 v21, v127 offset:1280
	ds_read_b32 v22, v127 offset:1536
	ds_read_b32 v23, v127 offset:1792
	ds_read_b32 v24, v127 offset:2048
	ds_read_b32 v25, v127 offset:2304
	ds_read_b32 v26, v127 offset:2560
	ds_read_b32 v27, v127 offset:2816
	ds_read_b32 v28, v127 offset:3072
	ds_read_b32 v29, v127 offset:3328
	ds_read_b32 v30, v127 offset:3584
	ds_read_b32 v31, v127 offset:3840
	ds_read_b32 v32, v127 offset:4096
	s_waitcnt lgkmcnt(0)
	v_add_f32_e32 v0, v0, v16
	v_add_f32_e32 v1, v1, v17
	v_add_f32_e32 v2, v2, v18
	v_add_f32_e32 v3, v3, v19
	v_add_f32_e32 v4, v4, v20
	v_add_f32_e32 v5, v5, v21
	v_add_f32_e32 v6, v6, v22
	v_add_f32_e32 v7, v7, v23
	v_add_f32_e32 v8, v8, v24
	v_add_f32_e32 v9, v9, v25
	v_add_f32_e32 v10, v10, v26
	v_add_f32_e32 v11, v11, v27
	v_add_f32_e32 v12, v12, v28
	v_add_f32_e32 v13, v13, v29
	v_add_f32_e32 v14, v14, v30
	v_add_f32_e32 v15, v15, v31
	v_add_f32_e32 v80, v80, v32
	s_nop 15
	s_nop 1
	ds_write2_b32 v85, v0, v1 offset1:1
	ds_write2_b32 v85, v2, v3 offset0:2 offset1:3
	ds_write2_b32 v85, v4, v5 offset0:8 offset1:9
	ds_write2_b32 v85, v6, v7 offset0:10 offset1:11
	ds_write2_b32 v85, v8, v9 offset0:16 offset1:17
	ds_write2_b32 v85, v10, v11 offset0:18 offset1:19
	ds_write2_b32 v85, v12, v13 offset0:24 offset1:25
	ds_write2_b32 v85, v14, v15 offset0:26 offset1:27
	v_mov_b32_e32 v0, v80
	v_add_u32_e32 v34, s10, v84
	v_ashrrev_i32_e32 v35, 31, v34
	ds_write_b32 v86, v0 offset:36864
	global_load_dwordx4 v[200:203], v87, s[38:39] offset:48
	global_load_dwordx4 v[204:207], v87, s[38:39] offset:32
	global_load_dwordx4 v[208:211], v87, s[38:39] offset:16
	global_load_dwordx4 v[212:215], v87, s[38:39]
	global_load_dwordx4 v[216:219], v87, s[38:39] offset:112
	global_load_dwordx4 v[220:223], v87, s[38:39] offset:96
	global_load_dwordx4 v[224:227], v87, s[38:39] offset:80
	global_load_dwordx4 v[228:231], v87, s[38:39] offset:64
	s_waitcnt lgkmcnt(0)
	s_barrier
	s_and_saveexec_b64 s[46:47], s[6:7]
	s_cbranch_execz .LBB0_986
; __global__ void __launch_bounds__(512, 2) fwd_kernel(Params p) {
;     ...
;             if (tid < 64) {
;                 const int t2 = tid >> 5, jj = tid & 31, tok = blk * 64 + tid;
;                 float s = 0.f;
; #pragma unroll
;                 for (int q = 0; q < 4; ++q) s += ssq[((q * 2 + t2) * 32 + jj) * 2] + ssq[((q * 2 + t2) * 32 + jj) * 2 + 1];
;                 const float rstd = rsqrtf(s * (1.f / DM) + RMS_EPS);
;                 RS2[tok] = rstd;
;                 float lgv[NE];
; #pragma unroll
;                 for (int e = 0; e < NE; ++e) { float v = 0.f;
; #pragma unroll
;                     for (int q = 0; q < 4; ++q) v += part[((q * 2 + t2) * 32 + jj) * 33 + e];
;                     lgv[e] = v * rstd + p.in[I_BR][e]; }
	ds_read2st64_b64 v[0:3], v136 offset0:72 offset1:73
	ds_read2_b32 v[18:19], v135 offset1:1
	s_movk_i32 s0, 0x80
	s_waitcnt lgkmcnt(1)
	v_mov_b32_e32 v4, v0
	v_mov_b32_e32 v5, v2
	v_mov_b32_e32 v2, v1
	v_pk_add_f32 v[0:1], v[4:5], v[2:3]
	s_nop 0
	v_add_f32_e32 v0, 0, v0
	v_add_f32_e32 v6, v0, v1
	ds_read2st64_b64 v[0:3], v136 offset0:74 offset1:75
	s_waitcnt lgkmcnt(0)
	v_mov_b32_e32 v4, v0
	v_mov_b32_e32 v5, v2
	v_mov_b32_e32 v2, v1
	v_pk_add_f32 v[0:1], v[4:5], v[2:3]
	s_nop 0
	v_add_f32_e32 v0, v6, v0
	v_add_f32_e32 v0, v0, v1
	v_fmamk_f32 v0, v0, 0x3a000000, v137
	v_cmp_gt_f32_e32 vcc, s57, v0
	v_mul_f32_e32 v1, 0x4b800000, v0
	s_nop 0
	v_cndmask_b32_e32 v0, v0, v1, vcc
	v_rsq_f32_e32 v0, v0
	s_nop 0
	v_mul_f32_e32 v1, 0x45800000, v0
	v_cndmask_b32_e32 v16, v0, v1, vcc
	v_mov_b32_e32 v244, v16
	v_lshl_add_u64 v[0:1], v[34:35], 2, s[44:45]
	global_store_dword v[0:1], v16, off
	v_add_u32_e32 v1, 0x2100, v135
	ds_read2_b32 v[20:21], v1 offset1:1
	v_add_u32_e32 v1, 0x4200, v135
	ds_read2_b32 v[22:23], v1 offset1:1
	v_add_u32_e32 v1, 0x6300, v135
	ds_read2_b32 v[24:25], v1 offset1:1
	v_add_f32_e32 v0, 0, v18
	s_waitcnt lgkmcnt(2)
	v_add_f32_e32 v0, v0, v20
	s_waitcnt lgkmcnt(1)
	v_add_f32_e32 v0, v0, v22
	s_waitcnt lgkmcnt(0)
	v_add_f32_e32 v17, v0, v24
	s_waitcnt vmcnt(1)
	v_mov_b32_e32 v0, v200
	v_mov_b32_e32 v1, v201
	v_mov_b32_e32 v2, v202
	v_mov_b32_e32 v3, v203
	v_mov_b32_e32 v4, v204
	v_mov_b32_e32 v5, v205
	v_mov_b32_e32 v6, v206
	v_mov_b32_e32 v7, v207
	v_mov_b32_e32 v8, v208
	v_mov_b32_e32 v9, v209
	v_mov_b32_e32 v10, v210
	v_mov_b32_e32 v11, v211
	v_mov_b32_e32 v12, v212
	v_mov_b32_e32 v13, v213
	v_mov_b32_e32 v14, v214
	v_mov_b32_e32 v15, v215
	v_fma_f32 v37, v16, v17, v12
	v_add_f32_e32 v12, 0, v19
	v_add_f32_e32 v12, v12, v21
	v_add_f32_e32 v12, v12, v23
	v_add_f32_e32 v12, v12, v25
	v_fma_f32 v36, v16, v12, v13
	ds_read2_b32 v[12:13], v135 offset0:2 offset1:3
	v_add_u32_e32 v17, 0x2108, v135
	ds_read2_b32 v[18:19], v17 offset1:1
	v_add_u32_e32 v17, 0x4208, v135
	ds_read2_b32 v[20:21], v17 offset1:1
	v_add_u32_e32 v17, 0x6308, v135
	ds_read2_b32 v[22:23], v17 offset1:1
	s_waitcnt lgkmcnt(3)
	v_add_f32_e32 v12, 0, v12
	s_waitcnt lgkmcnt(2)
	v_add_f32_e32 v12, v12, v18
	s_waitcnt lgkmcnt(1)
	v_add_f32_e32 v12, v12, v20
	v_add_u32_e32 v17, 0x2110, v135
	s_waitcnt lgkmcnt(0)
	v_add_f32_e32 v12, v12, v22
	v_fma_f32 v14, v16, v12, v14
	v_add_f32_e32 v12, 0, v13
	v_add_f32_e32 v12, v12, v19
	v_add_f32_e32 v12, v12, v21
	v_add_f32_e32 v12, v12, v23
	v_fmac_f32_e32 v15, v16, v12
	ds_read2_b32 v[12:13], v135 offset0:4 offset1:5
	ds_read2_b32 v[18:19], v17 offset1:1
	v_add_u32_e32 v17, 0x4210, v135
	ds_read2_b32 v[20:21], v17 offset1:1
	v_add_u32_e32 v17, 0x6310, v135
	ds_read2_b32 v[22:23], v17 offset1:1
	s_waitcnt lgkmcnt(3)
	v_add_f32_e32 v12, 0, v12
	s_waitcnt lgkmcnt(2)
	v_add_f32_e32 v12, v12, v18
	s_waitcnt lgkmcnt(1)
	v_add_f32_e32 v12, v12, v20
	v_cmp_lg_f32_e32 vcc, s58, v37
	s_waitcnt lgkmcnt(0)
	v_add_f32_e32 v12, v12, v22
	v_fma_f32 v39, v16, v12, v8
	v_add_f32_e32 v8, 0, v13
	v_add_f32_e32 v8, v8, v19
	v_add_f32_e32 v8, v8, v21
	v_add_f32_e32 v8, v8, v23
	v_fma_f32 v38, v16, v8, v9
	ds_read2_b32 v[8:9], v135 offset0:6 offset1:7
	v_add_u32_e32 v12, 0x2118, v135
	ds_read2_b32 v[12:13], v12 offset1:1
	s_waitcnt lgkmcnt(1)
	v_add_f32_e32 v8, 0, v8
	s_waitcnt lgkmcnt(0)
	v_add_f32_e32 v8, v8, v12
	v_add_u32_e32 v12, 0x4218, v135
	ds_read2_b32 v[18:19], v12 offset1:1
	v_add_u32_e32 v12, 0x6318, v135
	ds_read2_b32 v[20:21], v12 offset1:1
	v_add_u32_e32 v12, 0x2120, v135
	s_waitcnt lgkmcnt(1)
	v_add_f32_e32 v8, v8, v18
	s_waitcnt lgkmcnt(0)
	v_add_f32_e32 v8, v8, v20
	v_fma_f32 v10, v16, v8, v10
	v_add_f32_e32 v8, 0, v9
	v_add_f32_e32 v8, v8, v13
	v_add_f32_e32 v8, v8, v19
	v_add_f32_e32 v8, v8, v21
	v_fmac_f32_e32 v11, v16, v8
	ds_read2_b32 v[8:9], v135 offset0:8 offset1:9
	ds_read2_b32 v[12:13], v12 offset1:1
	s_waitcnt lgkmcnt(1)
	v_add_f32_e32 v8, 0, v8
	s_waitcnt lgkmcnt(0)
	v_add_f32_e32 v8, v8, v12
	v_add_u32_e32 v12, 0x4220, v135
	ds_read2_b32 v[18:19], v12 offset1:1
	v_add_u32_e32 v12, 0x6320, v135
	ds_read2_b32 v[20:21], v12 offset1:1
	s_waitcnt lgkmcnt(1)
	v_add_f32_e32 v8, v8, v18
	s_waitcnt lgkmcnt(0)
	v_add_f32_e32 v8, v8, v20
	v_fma_f32 v41, v16, v8, v4
	v_add_f32_e32 v4, 0, v9
	v_add_f32_e32 v4, v4, v13
	v_add_f32_e32 v4, v4, v19
	v_add_f32_e32 v4, v4, v21
	v_fma_f32 v40, v16, v4, v5
	ds_read2_b32 v[4:5], v135 offset0:10 offset1:11
	v_add_u32_e32 v8, 0x2128, v135
	ds_read2_b32 v[8:9], v8 offset1:1
	s_waitcnt lgkmcnt(1)
	v_add_f32_e32 v4, 0, v4
	s_waitcnt lgkmcnt(0)
	v_add_f32_e32 v4, v4, v8
	v_add_u32_e32 v8, 0x4228, v135
	ds_read2_b32 v[12:13], v8 offset1:1
	v_add_u32_e32 v8, 0x6328, v135
	ds_read2_b32 v[18:19], v8 offset1:1
	v_add_u32_e32 v8, 0x2130, v135
	s_waitcnt lgkmcnt(1)
	v_add_f32_e32 v4, v4, v12
	s_waitcnt lgkmcnt(0)
	v_add_f32_e32 v4, v4, v18
	v_fma_f32 v6, v16, v4, v6
	v_add_f32_e32 v4, 0, v5
	v_add_f32_e32 v4, v4, v9
	v_add_f32_e32 v4, v4, v13
	v_add_f32_e32 v4, v4, v19
	v_fmac_f32_e32 v7, v16, v4
	ds_read2_b32 v[4:5], v135 offset0:12 offset1:13
	ds_read2_b32 v[8:9], v8 offset1:1
	s_waitcnt lgkmcnt(1)
	v_add_f32_e32 v4, 0, v4
	s_waitcnt lgkmcnt(0)
	v_add_f32_e32 v4, v4, v8
	v_add_u32_e32 v8, 0x4230, v135
	ds_read2_b32 v[12:13], v8 offset1:1
	v_add_u32_e32 v8, 0x6330, v135
	ds_read2_b32 v[18:19], v8 offset1:1
	s_waitcnt lgkmcnt(1)
	v_add_f32_e32 v4, v4, v12
	s_waitcnt lgkmcnt(0)
	v_add_f32_e32 v4, v4, v18
	v_fma_f32 v43, v16, v4, v0
	v_add_f32_e32 v0, 0, v5
	v_add_f32_e32 v0, v0, v9
	v_add_f32_e32 v0, v0, v13
	v_add_f32_e32 v0, v0, v19
	v_fma_f32 v42, v16, v0, v1
	ds_read2_b32 v[0:1], v135 offset0:14 offset1:15
	v_add_u32_e32 v4, 0x2138, v135
	ds_read2_b32 v[4:5], v4 offset1:1
	s_waitcnt lgkmcnt(1)
; __global__ void __launch_bounds__(512, 2) fwd_kernel(Params p) {
;     ...
;                 float lgv[NE];
; #pragma unroll
;                 for (int e = 0; e < NE; ++e) { float v = 0.f;
; #pragma unroll
;                     for (int q = 0; q < 4; ++q) v += part[((q * 2 + t2) * 32 + jj) * 33 + e];
;                     lgv[e] = v * rstd + p.in[I_BR][e]; }
	v_add_f32_e32 v0, 0, v0
	s_waitcnt lgkmcnt(0)
	v_add_f32_e32 v0, v0, v4
	v_add_u32_e32 v4, 0x4238, v135
	ds_read2_b32 v[8:9], v4 offset1:1
	v_add_u32_e32 v4, 0x6338, v135
	ds_read2_b32 v[12:13], v4 offset1:1
	v_add_u32_e32 v4, 0x2140, v135
	s_waitcnt lgkmcnt(1)
	v_add_f32_e32 v0, v0, v8
	s_waitcnt lgkmcnt(0)
	v_add_f32_e32 v0, v0, v12
	v_fma_f32 v2, v16, v0, v2
	v_add_f32_e32 v0, 0, v1
	v_add_f32_e32 v0, v0, v5
	v_add_f32_e32 v0, v0, v9
	v_add_f32_e32 v0, v0, v13
	v_fmac_f32_e32 v3, v16, v0
	ds_read2_b32 v[0:1], v135 offset0:16 offset1:17
	ds_read2_b32 v[4:5], v4 offset1:1
	s_waitcnt lgkmcnt(1)
	v_add_f32_e32 v0, 0, v0
	s_waitcnt lgkmcnt(0)
	v_add_f32_e32 v0, v0, v4
	v_add_u32_e32 v4, 0x4240, v135
	ds_read2_b32 v[8:9], v4 offset1:1
	v_add_u32_e32 v4, 0x6340, v135
	ds_read2_b32 v[12:13], v4 offset1:1
	v_mov_b32_e32 v18, v216
	v_mov_b32_e32 v19, v217
	v_mov_b32_e32 v20, v218
	v_mov_b32_e32 v21, v219
	v_mov_b32_e32 v22, v220
	v_mov_b32_e32 v23, v221
	v_mov_b32_e32 v24, v222
	v_mov_b32_e32 v25, v223
	v_mov_b32_e32 v26, v224
	v_mov_b32_e32 v27, v225
	v_mov_b32_e32 v28, v226
	v_mov_b32_e32 v29, v227
	v_mov_b32_e32 v30, v228
	v_mov_b32_e32 v31, v229
	v_mov_b32_e32 v32, v230
	v_mov_b32_e32 v33, v231
	s_waitcnt lgkmcnt(1)
	v_add_f32_e32 v0, v0, v8
	s_waitcnt lgkmcnt(0)
	v_add_f32_e32 v0, v0, v12
	v_fma_f32 v4, v16, v0, v30
	v_add_f32_e32 v0, 0, v1
	v_add_f32_e32 v0, v0, v5
	v_add_f32_e32 v0, v0, v9
	ds_read2_b32 v[8:9], v135 offset0:18 offset1:19
	v_add_u32_e32 v5, 0x2148, v135
	v_add_f32_e32 v0, v0, v13
	ds_read2_b32 v[12:13], v5 offset1:1
	v_add_u32_e32 v5, 0x4248, v135
	v_fma_f32 v0, v16, v0, v31
	ds_read2_b32 v[30:31], v5 offset1:1
	v_add_u32_e32 v5, 0x6348, v135
	ds_read2_b32 v[44:45], v5 offset1:1
	s_waitcnt lgkmcnt(3)
	v_add_f32_e32 v1, 0, v8
	v_add_f32_e32 v5, 0, v9
	ds_read2_b32 v[8:9], v135 offset0:20 offset1:21
	s_waitcnt lgkmcnt(3)
	v_add_f32_e32 v5, v5, v13
	s_waitcnt lgkmcnt(2)
	v_add_f32_e32 v5, v5, v31
	s_waitcnt lgkmcnt(1)
	v_add_f32_e32 v5, v5, v45
	v_fmac_f32_e32 v33, v16, v5
	s_waitcnt lgkmcnt(0)
	v_add_f32_e32 v5, 0, v8
	v_add_u32_e32 v8, 0x2150, v135
	v_add_f32_e32 v1, v1, v12
	ds_read2_b32 v[12:13], v8 offset1:1
	v_add_u32_e32 v8, 0x4250, v135
	v_add_f32_e32 v1, v1, v30
	ds_read2_b32 v[30:31], v8 offset1:1
	v_add_u32_e32 v8, 0x6350, v135
	v_add_f32_e32 v1, v1, v44
	ds_read2_b32 v[44:45], v8 offset1:1
	s_waitcnt lgkmcnt(2)
	v_add_f32_e32 v5, v5, v12
	s_waitcnt lgkmcnt(1)
	v_add_f32_e32 v5, v5, v30
	v_fma_f32 v1, v16, v1, v32
	s_waitcnt lgkmcnt(0)
	v_add_f32_e32 v5, v5, v44
	v_fma_f32 v8, v16, v5, v26
	v_add_f32_e32 v5, 0, v9
	v_add_f32_e32 v5, v5, v13
	ds_read2_b32 v[12:13], v135 offset0:22 offset1:23
	v_add_f32_e32 v5, v5, v31
	v_add_f32_e32 v5, v5, v45
	v_fma_f32 v5, v16, v5, v27
	s_waitcnt lgkmcnt(0)
	v_add_f32_e32 v9, 0, v12
	v_add_u32_e32 v12, 0x2158, v135
	ds_read2_b32 v[26:27], v12 offset1:1
	v_add_u32_e32 v12, 0x4258, v135
	ds_read2_b32 v[30:31], v12 offset1:1
	v_add_u32_e32 v12, 0x6358, v135
	ds_read2_b32 v[44:45], v12 offset1:1
	v_add_f32_e32 v12, 0, v13
	s_waitcnt lgkmcnt(2)
	v_add_f32_e32 v9, v9, v26
	v_add_f32_e32 v12, v12, v27
	ds_read2_b32 v[26:27], v135 offset0:24 offset1:25
	v_add_u32_e32 v13, 0x2160, v135
	s_waitcnt lgkmcnt(2)
	v_add_f32_e32 v9, v9, v30
	v_add_f32_e32 v12, v12, v31
	ds_read2_b32 v[30:31], v13 offset1:1
	v_add_u32_e32 v13, 0x4260, v135
	s_waitcnt lgkmcnt(2)
	v_add_f32_e32 v9, v9, v44
	v_add_f32_e32 v12, v12, v45
	ds_read2_b32 v[44:45], v13 offset1:1
	v_add_u32_e32 v13, 0x6360, v135
	ds_read2_b32 v[46:47], v13 offset1:1
	v_fmac_f32_e32 v29, v16, v12
	s_waitcnt lgkmcnt(3)
	v_add_f32_e32 v12, 0, v26
	s_waitcnt lgkmcnt(2)
	v_add_f32_e32 v12, v12, v30
	s_waitcnt lgkmcnt(1)
	v_add_f32_e32 v12, v12, v44
	s_waitcnt lgkmcnt(0)
	v_add_f32_e32 v12, v12, v46
	v_fma_f32 v13, v16, v12, v22
	v_add_f32_e32 v12, 0, v27
	v_add_f32_e32 v12, v12, v31
	v_add_f32_e32 v12, v12, v45
	v_add_f32_e32 v12, v12, v47
	v_fma_f32 v12, v16, v12, v23
	ds_read2_b32 v[22:23], v135 offset0:26 offset1:27
	v_fma_f32 v9, v16, v9, v28
	s_waitcnt lgkmcnt(0)
	v_add_f32_e32 v17, 0, v22
	v_add_u32_e32 v22, 0x2168, v135
	ds_read2_b32 v[26:27], v22 offset1:1
	v_add_u32_e32 v22, 0x4268, v135
	ds_read2_b32 v[30:31], v22 offset1:1
	v_add_u32_e32 v22, 0x6368, v135
	ds_read2_b32 v[44:45], v22 offset1:1
	s_waitcnt lgkmcnt(2)
	v_add_f32_e32 v17, v17, v26
	s_waitcnt lgkmcnt(1)
	v_add_f32_e32 v17, v17, v30
	s_waitcnt lgkmcnt(0)
	v_add_f32_e32 v17, v17, v44
	v_fma_f32 v22, v16, v17, v24
	v_add_f32_e32 v17, 0, v23
	v_add_f32_e32 v17, v17, v27
	ds_read2_b32 v[26:27], v135 offset0:28 offset1:29
	v_add_u32_e32 v23, 0x2170, v135
	v_add_f32_e32 v17, v17, v31
	ds_read2_b32 v[30:31], v23 offset1:1
	v_add_u32_e32 v23, 0x4270, v135
	v_add_f32_e32 v17, v17, v45
	ds_read2_b32 v[44:45], v23 offset1:1
	v_add_u32_e32 v23, 0x6370, v135
	ds_read2_b32 v[46:47], v23 offset1:1
	v_fmac_f32_e32 v25, v16, v17
	s_waitcnt lgkmcnt(3)
	v_add_f32_e32 v17, 0, v26
	s_waitcnt lgkmcnt(2)
	v_add_f32_e32 v17, v17, v30
	s_waitcnt lgkmcnt(1)
	v_add_f32_e32 v17, v17, v44
	s_waitcnt lgkmcnt(0)
	v_add_f32_e32 v17, v17, v46
	v_fma_f32 v23, v16, v17, v18
	v_add_f32_e32 v17, 0, v27
	ds_read2_b32 v[26:27], v135 offset0:30 offset1:31
	v_add_u32_e32 v18, 0x2178, v135
	v_add_f32_e32 v17, v17, v31
	ds_read2_b32 v[30:31], v18 offset1:1
	v_add_u32_e32 v18, 0x4278, v135
	v_add_f32_e32 v17, v17, v45
	ds_read2_b32 v[44:45], v18 offset1:1
	v_add_u32_e32 v18, 0x6378, v135
	v_add_f32_e32 v17, v17, v47
	ds_read2_b32 v[46:47], v18 offset1:1
	v_fma_f32 v19, v16, v17, v19
	s_waitcnt lgkmcnt(3)
	v_add_f32_e32 v17, 0, v26
	s_waitcnt lgkmcnt(2)
	v_add_f32_e32 v17, v17, v30
	s_waitcnt lgkmcnt(1)
; __global__ void __launch_bounds__(512, 2) fwd_kernel(Params p) {
;     ...
;                 float lgv[NE];
; #pragma unroll
;                 for (int e = 0; e < NE; ++e) { float v = 0.f;
; #pragma unroll
;                     for (int q = 0; q < 4; ++q) v += part[((q * 2 + t2) * 32 + jj) * 33 + e];
;                     lgv[e] = v * rstd + p.in[I_BR][e]; }
;                 unsigned mask = 0u; float tv[4];
; #pragma unroll
;                 for (int k = 0; k < 4; ++k) { float best = -__builtin_inff(); int be = 0;
; #pragma unroll
;                     for (int e = 0; e < NE; ++e) { const bool take = !((mask >> e) & 1u) && lgv[e] > best; best = take ? lgv[e] : best; be = take ? e : be; }
	v_add_f32_e32 v17, v17, v44
	s_waitcnt lgkmcnt(0)
	v_add_f32_e32 v17, v17, v46
	v_fma_f32 v20, v16, v17, v20
	v_add_f32_e32 v17, 0, v27
	v_add_f32_e32 v17, v17, v31
	v_add_f32_e32 v17, v17, v45
	v_add_f32_e32 v17, v17, v47
	v_fmac_f32_e32 v21, v16, v17
	v_cndmask_b32_e32 v16, v139, v37, vcc
	v_cmp_gt_f32_e32 vcc, v36, v16
	s_nop 1
	v_cndmask_b32_e32 v16, v16, v36, vcc
	v_cndmask_b32_e64 v17, 0, 1, vcc
	v_cmp_gt_f32_e32 vcc, v14, v16
	s_nop 1
	v_cndmask_b32_e32 v16, v16, v14, vcc
	v_cndmask_b32_e64 v17, v17, 2, vcc
	v_cmp_gt_f32_e32 vcc, v15, v16
	s_nop 1
	v_cndmask_b32_e32 v16, v16, v15, vcc
	v_cndmask_b32_e64 v17, v17, 3, vcc
	v_cmp_gt_f32_e32 vcc, v39, v16
	s_nop 1
	v_cndmask_b32_e32 v16, v16, v39, vcc
	v_cndmask_b32_e64 v17, v17, 4, vcc
	v_cmp_gt_f32_e32 vcc, v38, v16
	s_nop 1
	v_cndmask_b32_e32 v16, v16, v38, vcc
	v_cndmask_b32_e64 v17, v17, 5, vcc
	v_cmp_gt_f32_e32 vcc, v10, v16
	s_nop 1
	v_cndmask_b32_e32 v16, v16, v10, vcc
	v_cndmask_b32_e64 v17, v17, 6, vcc
	v_cmp_gt_f32_e32 vcc, v11, v16
	s_nop 1
	v_cndmask_b32_e32 v16, v16, v11, vcc
	v_cndmask_b32_e64 v17, v17, 7, vcc
	v_cmp_gt_f32_e32 vcc, v41, v16
	s_nop 1
	v_cndmask_b32_e32 v16, v16, v41, vcc
	v_cndmask_b32_e64 v17, v17, 8, vcc
	v_cmp_gt_f32_e32 vcc, v40, v16
	s_nop 1
	v_cndmask_b32_e32 v16, v16, v40, vcc
	v_cndmask_b32_e64 v17, v17, 9, vcc
	v_cmp_gt_f32_e32 vcc, v6, v16
	s_nop 1
	v_cndmask_b32_e32 v16, v16, v6, vcc
	v_cndmask_b32_e64 v17, v17, 10, vcc
	v_cmp_gt_f32_e32 vcc, v7, v16
	s_nop 1
	v_cndmask_b32_e32 v16, v16, v7, vcc
	v_cndmask_b32_e64 v17, v17, 11, vcc
	v_cmp_gt_f32_e32 vcc, v43, v16
	s_nop 1
	v_cndmask_b32_e32 v16, v16, v43, vcc
	v_cndmask_b32_e64 v17, v17, 12, vcc
	v_cmp_gt_f32_e32 vcc, v42, v16
	s_nop 1
	v_cndmask_b32_e32 v16, v16, v42, vcc
	v_cndmask_b32_e64 v17, v17, 13, vcc
	v_cmp_gt_f32_e32 vcc, v2, v16
	s_nop 1
	v_cndmask_b32_e32 v16, v16, v2, vcc
	v_cndmask_b32_e64 v17, v17, 14, vcc
	v_cmp_gt_f32_e32 vcc, v3, v16
	s_nop 1
	v_cndmask_b32_e32 v16, v16, v3, vcc
	v_cndmask_b32_e64 v17, v17, 15, vcc
	v_cmp_gt_f32_e32 vcc, v4, v16
	s_nop 1
	v_cndmask_b32_e32 v16, v16, v4, vcc
	v_cndmask_b32_e64 v17, v17, 16, vcc
	v_cmp_gt_f32_e32 vcc, v0, v16
	s_nop 1
	v_cndmask_b32_e32 v16, v16, v0, vcc
	v_cndmask_b32_e64 v17, v17, 17, vcc
	v_cmp_gt_f32_e32 vcc, v1, v16
	s_nop 1
	v_cndmask_b32_e32 v16, v16, v1, vcc
	v_cndmask_b32_e64 v17, v17, 18, vcc
	v_cmp_gt_f32_e32 vcc, v33, v16
	s_nop 1
	v_cndmask_b32_e32 v16, v16, v33, vcc
	v_cndmask_b32_e64 v17, v17, 19, vcc
	v_cmp_gt_f32_e32 vcc, v8, v16
	s_nop 1
	v_cndmask_b32_e32 v16, v16, v8, vcc
	v_cndmask_b32_e64 v17, v17, 20, vcc
	v_cmp_gt_f32_e32 vcc, v5, v16
	s_nop 1
	v_cndmask_b32_e32 v16, v16, v5, vcc
	v_cndmask_b32_e64 v17, v17, 21, vcc
	v_cmp_gt_f32_e32 vcc, v9, v16
	s_nop 1
	v_cndmask_b32_e32 v16, v16, v9, vcc
	v_cndmask_b32_e64 v17, v17, 22, vcc
	v_cmp_gt_f32_e32 vcc, v29, v16
	s_nop 1
	v_cndmask_b32_e32 v16, v16, v29, vcc
	v_cndmask_b32_e64 v17, v17, 23, vcc
	v_cmp_gt_f32_e32 vcc, v13, v16
	s_nop 1
	v_cndmask_b32_e32 v16, v16, v13, vcc
	v_cndmask_b32_e64 v17, v17, 24, vcc
	v_cmp_gt_f32_e32 vcc, v12, v16
	s_nop 1
	v_cndmask_b32_e32 v16, v16, v12, vcc
	v_cndmask_b32_e64 v17, v17, 25, vcc
	v_cmp_gt_f32_e32 vcc, v22, v16
	s_nop 1
	v_cndmask_b32_e32 v16, v16, v22, vcc
	v_cndmask_b32_e64 v17, v17, 26, vcc
	v_cmp_gt_f32_e32 vcc, v25, v16
	s_nop 1
	v_cndmask_b32_e32 v16, v16, v25, vcc
	v_cndmask_b32_e64 v17, v17, 27, vcc
	v_cmp_gt_f32_e32 vcc, v23, v16
	s_nop 1
	v_cndmask_b32_e32 v16, v16, v23, vcc
	v_cndmask_b32_e64 v17, v17, 28, vcc
	v_cmp_gt_f32_e32 vcc, v19, v16
	s_nop 1
	v_cndmask_b32_e32 v16, v16, v19, vcc
	v_cndmask_b32_e64 v17, v17, 29, vcc
	v_cmp_gt_f32_e32 vcc, v20, v16
	s_nop 1
	v_cndmask_b32_e32 v18, v16, v20, vcc
	v_cndmask_b32_e64 v17, v17, 30, vcc
	v_cmp_gt_f32_e32 vcc, v21, v18
	s_nop 1
	v_cndmask_b32_e64 v16, v17, 31, vcc
	v_cndmask_b32_e32 v24, v18, v21, vcc
	v_cmp_eq_u32_e64 s[10:11], 0, v16
	v_cmp_nlg_f32_e32 vcc, s58, v37
	v_lshlrev_b32_e64 v18, v16, 1
	s_or_b64 s[10:11], s[10:11], vcc
	v_cndmask_b32_e64 v17, v37, v139, s[10:11]
	v_and_b32_e32 v26, 2, v18
	v_cmp_eq_u32_e64 s[10:11], 0, v26
	v_cmp_gt_f32_e64 s[12:13], v36, v17
	s_and_b64 s[10:11], s[10:11], s[12:13]
	v_cndmask_b32_e64 v17, v17, v36, s[10:11]
	v_and_b32_e32 v27, 4, v18
	v_cndmask_b32_e64 v26, 0, 1, s[10:11]
	v_cmp_eq_u32_e64 s[10:11], 0, v27
	v_cmp_gt_f32_e64 s[12:13], v14, v17
	s_and_b64 s[10:11], s[10:11], s[12:13]
	v_cndmask_b32_e64 v17, v17, v14, s[10:11]
	v_and_b32_e32 v27, 8, v18
	v_cndmask_b32_e64 v26, v26, 2, s[10:11]
	v_cmp_eq_u32_e64 s[10:11], 0, v27
	v_cmp_gt_f32_e64 s[12:13], v15, v17
	s_and_b64 s[10:11], s[10:11], s[12:13]
	v_cndmask_b32_e64 v17, v17, v15, s[10:11]
	v_and_b32_e32 v27, 16, v18
	v_cndmask_b32_e64 v26, v26, 3, s[10:11]
	v_cmp_eq_u32_e64 s[10:11], 0, v27
	v_cmp_gt_f32_e64 s[12:13], v39, v17
	s_and_b64 s[10:11], s[10:11], s[12:13]
	v_cndmask_b32_e64 v17, v17, v39, s[10:11]
	v_and_b32_e32 v27, 32, v18
	v_cndmask_b32_e64 v26, v26, 4, s[10:11]
	v_cmp_eq_u32_e64 s[10:11], 0, v27
	v_cmp_gt_f32_e64 s[12:13], v38, v17
	s_and_b64 s[10:11], s[10:11], s[12:13]
	v_cndmask_b32_e64 v17, v17, v38, s[10:11]
	v_and_b32_e32 v27, 64, v18
	v_cndmask_b32_e64 v26, v26, 5, s[10:11]
	v_cmp_eq_u32_e64 s[10:11], 0, v27
	v_cmp_gt_f32_e64 s[12:13], v10, v17
	s_and_b64 s[10:11], s[10:11], s[12:13]
	v_cndmask_b32_e64 v17, v17, v10, s[10:11]
	v_and_b32_e32 v27, 0x80, v18
	v_cndmask_b32_e64 v26, v26, 6, s[10:11]
	v_cmp_eq_u32_e64 s[10:11], 0, v27
	v_cmp_gt_f32_e64 s[12:13], v11, v17
	s_and_b64 s[10:11], s[10:11], s[12:13]
	v_cndmask_b32_e64 v17, v17, v11, s[10:11]
	v_and_b32_e32 v27, 0x100, v18
	v_cndmask_b32_e64 v26, v26, 7, s[10:11]
; __global__ void __launch_bounds__(512, 2) fwd_kernel(Params p) {
;     ...
;                 unsigned mask = 0u; float tv[4];
; #pragma unroll
;                 for (int k = 0; k < 4; ++k) { float best = -__builtin_inff(); int be = 0;
; #pragma unroll
;                     for (int e = 0; e < NE; ++e) { const bool take = !((mask >> e) & 1u) && lgv[e] > best; best = take ? lgv[e] : best; be = take ? e : be; }
;                     mask |= 1u << be; tv[k] = best; te[k] = be; }
	v_cmp_eq_u32_e64 s[10:11], 0, v27
	v_cmp_gt_f32_e64 s[12:13], v41, v17
	s_and_b64 s[10:11], s[10:11], s[12:13]
	v_cndmask_b32_e64 v17, v17, v41, s[10:11]
	v_and_b32_e32 v27, 0x200, v18
	v_cndmask_b32_e64 v26, v26, 8, s[10:11]
	v_cmp_eq_u32_e64 s[10:11], 0, v27
	v_cmp_gt_f32_e64 s[12:13], v40, v17
	s_and_b64 s[10:11], s[10:11], s[12:13]
	v_cndmask_b32_e64 v17, v17, v40, s[10:11]
	v_and_b32_e32 v27, 0x400, v18
	v_cndmask_b32_e64 v26, v26, 9, s[10:11]
	v_cmp_eq_u32_e64 s[10:11], 0, v27
	v_cmp_gt_f32_e64 s[12:13], v6, v17
	s_and_b64 s[10:11], s[10:11], s[12:13]
	v_cndmask_b32_e64 v17, v17, v6, s[10:11]
	v_and_b32_e32 v27, 0x800, v18
	v_cndmask_b32_e64 v26, v26, 10, s[10:11]
	v_cmp_eq_u32_e64 s[10:11], 0, v27
	v_cmp_gt_f32_e64 s[12:13], v7, v17
	s_and_b64 s[10:11], s[10:11], s[12:13]
	v_cndmask_b32_e64 v17, v17, v7, s[10:11]
	v_and_b32_e32 v27, 0x1000, v18
	v_cndmask_b32_e64 v26, v26, 11, s[10:11]
	v_cmp_eq_u32_e64 s[10:11], 0, v27
	v_cmp_gt_f32_e64 s[12:13], v43, v17
	s_and_b64 s[10:11], s[10:11], s[12:13]
	v_cndmask_b32_e64 v17, v17, v43, s[10:11]
	v_and_b32_e32 v27, 0x2000, v18
	v_cndmask_b32_e64 v26, v26, 12, s[10:11]
	v_cmp_eq_u32_e64 s[10:11], 0, v27
	v_cmp_gt_f32_e64 s[12:13], v42, v17
	s_and_b64 s[10:11], s[10:11], s[12:13]
	v_cndmask_b32_e64 v17, v17, v42, s[10:11]
	v_and_b32_e32 v27, 0x4000, v18
	v_cndmask_b32_e64 v26, v26, 13, s[10:11]
	v_cmp_eq_u32_e64 s[10:11], 0, v27
	v_cmp_gt_f32_e64 s[12:13], v2, v17
	s_and_b64 s[10:11], s[10:11], s[12:13]
	v_cndmask_b32_e64 v17, v17, v2, s[10:11]
	v_and_b32_e32 v27, 0x8000, v18
	v_cndmask_b32_e64 v26, v26, 14, s[10:11]
	v_cmp_eq_u32_e64 s[10:11], 0, v27
	v_cmp_gt_f32_e64 s[12:13], v3, v17
	s_and_b64 s[10:11], s[10:11], s[12:13]
	v_cndmask_b32_e64 v17, v17, v3, s[10:11]
	v_and_b32_e32 v27, 0x10000, v18
	v_cndmask_b32_e64 v26, v26, 15, s[10:11]
	v_cmp_eq_u32_e64 s[10:11], 0, v27
	v_cmp_gt_f32_e64 s[12:13], v4, v17
	s_and_b64 s[10:11], s[10:11], s[12:13]
	v_cndmask_b32_e64 v17, v17, v4, s[10:11]
	v_and_b32_e32 v27, 0x20000, v18
	v_cndmask_b32_e64 v26, v26, 16, s[10:11]
	v_cmp_eq_u32_e64 s[10:11], 0, v27
	v_cmp_gt_f32_e64 s[12:13], v0, v17
	s_and_b64 s[10:11], s[10:11], s[12:13]
	v_cndmask_b32_e64 v17, v17, v0, s[10:11]
	v_and_b32_e32 v27, 0x40000, v18
	v_cndmask_b32_e64 v26, v26, 17, s[10:11]
	v_cmp_eq_u32_e64 s[10:11], 0, v27
	v_cmp_gt_f32_e64 s[12:13], v1, v17
	s_and_b64 s[10:11], s[10:11], s[12:13]
	v_cndmask_b32_e64 v17, v17, v1, s[10:11]
	v_and_b32_e32 v27, 0x80000, v18
	v_cndmask_b32_e64 v26, v26, 18, s[10:11]
	v_cmp_eq_u32_e64 s[10:11], 0, v27
	v_cmp_gt_f32_e64 s[12:13], v33, v17
	s_and_b64 s[10:11], s[10:11], s[12:13]
	v_cndmask_b32_e64 v17, v17, v33, s[10:11]
	v_and_b32_e32 v27, 0x100000, v18
	v_cndmask_b32_e64 v26, v26, 19, s[10:11]
	v_cmp_eq_u32_e64 s[10:11], 0, v27
	v_cmp_gt_f32_e64 s[12:13], v8, v17
	s_and_b64 s[10:11], s[10:11], s[12:13]
	v_cndmask_b32_e64 v17, v17, v8, s[10:11]
	v_and_b32_e32 v27, 0x200000, v18
	v_cndmask_b32_e64 v26, v26, 20, s[10:11]
	v_cmp_eq_u32_e64 s[10:11], 0, v27
	v_cmp_gt_f32_e64 s[12:13], v5, v17
	s_and_b64 s[10:11], s[10:11], s[12:13]
	v_cndmask_b32_e64 v17, v17, v5, s[10:11]
	v_and_b32_e32 v27, 0x400000, v18
	v_cndmask_b32_e64 v26, v26, 21, s[10:11]
	v_cmp_eq_u32_e64 s[10:11], 0, v27
	v_cmp_gt_f32_e64 s[12:13], v9, v17
	s_and_b64 s[10:11], s[10:11], s[12:13]
	v_cndmask_b32_e64 v17, v17, v9, s[10:11]
	v_and_b32_e32 v27, 0x800000, v18
	v_cndmask_b32_e64 v26, v26, 22, s[10:11]
	v_cmp_eq_u32_e64 s[10:11], 0, v27
	v_cmp_gt_f32_e64 s[12:13], v29, v17
	s_and_b64 s[10:11], s[10:11], s[12:13]
	v_cndmask_b32_e64 v17, v17, v29, s[10:11]
	v_and_b32_e32 v27, 0x1000000, v18
	v_cndmask_b32_e64 v26, v26, 23, s[10:11]
	v_cmp_eq_u32_e64 s[10:11], 0, v27
	v_cmp_gt_f32_e64 s[12:13], v13, v17
	s_and_b64 s[10:11], s[10:11], s[12:13]
	v_cndmask_b32_e64 v17, v17, v13, s[10:11]
	v_and_b32_e32 v27, 0x2000000, v18
	v_cndmask_b32_e64 v26, v26, 24, s[10:11]
	v_cmp_eq_u32_e64 s[10:11], 0, v27
	v_cmp_gt_f32_e64 s[12:13], v12, v17
	s_and_b64 s[10:11], s[10:11], s[12:13]
	v_cndmask_b32_e64 v17, v17, v12, s[10:11]
	v_and_b32_e32 v27, 0x4000000, v18
	v_cndmask_b32_e64 v26, v26, 25, s[10:11]
	v_cmp_eq_u32_e64 s[10:11], 0, v27
	v_cmp_gt_f32_e64 s[12:13], v22, v17
	s_and_b64 s[10:11], s[10:11], s[12:13]
	v_cndmask_b32_e64 v17, v17, v22, s[10:11]
	v_and_b32_e32 v27, 0x8000000, v18
	v_cndmask_b32_e64 v26, v26, 26, s[10:11]
	v_cmp_eq_u32_e64 s[10:11], 0, v27
	v_cmp_gt_f32_e64 s[12:13], v25, v17
	s_and_b64 s[10:11], s[10:11], s[12:13]
	v_cndmask_b32_e64 v17, v17, v25, s[10:11]
	v_and_b32_e32 v27, 0x10000000, v18
	v_cndmask_b32_e64 v26, v26, 27, s[10:11]
	v_cmp_eq_u32_e64 s[10:11], 0, v27
	v_cmp_gt_f32_e64 s[12:13], v23, v17
	s_and_b64 s[10:11], s[10:11], s[12:13]
	v_cndmask_b32_e64 v17, v17, v23, s[10:11]
	v_and_b32_e32 v27, 0x20000000, v18
	v_cndmask_b32_e64 v26, v26, 28, s[10:11]
	v_cmp_eq_u32_e64 s[10:11], 0, v27
	v_cmp_gt_f32_e64 s[12:13], v19, v17
	s_and_b64 s[10:11], s[10:11], s[12:13]
	v_cndmask_b32_e64 v17, v17, v19, s[10:11]
	v_and_b32_e32 v27, 2.0, v18
	v_cndmask_b32_e64 v26, v26, 29, s[10:11]
	v_cmp_eq_u32_e64 s[10:11], 0, v27
	v_cmp_gt_f32_e64 s[12:13], v20, v17
	s_and_b64 s[10:11], s[10:11], s[12:13]
	v_cndmask_b32_e64 v27, v17, v20, s[10:11]
	v_cndmask_b32_e64 v26, v26, 30, s[10:11]
	v_cmp_ne_u32_e64 s[10:11], 31, v16
	v_cmp_gt_f32_e64 s[12:13], v21, v27
	s_and_b64 s[10:11], s[10:11], s[12:13]
	v_cndmask_b32_e64 v17, v26, 31, s[10:11]
	v_cndmask_b32_e64 v26, v27, v21, s[10:11]
	v_lshl_or_b32 v27, 1, v17, v18
	v_and_b32_e32 v18, 1, v27
	v_cmp_eq_u32_e64 s[10:11], 1, v18
	s_or_b64 s[10:11], s[10:11], vcc
	v_and_b32_e32 v28, 2, v27
	v_cndmask_b32_e64 v18, v37, v139, s[10:11]
; __global__ void __launch_bounds__(512, 2) fwd_kernel(Params p) {
;     ...
;                 unsigned mask = 0u; float tv[4];
; #pragma unroll
;                 for (int k = 0; k < 4; ++k) { float best = -__builtin_inff(); int be = 0;
; #pragma unroll
;                     for (int e = 0; e < NE; ++e) { const bool take = !((mask >> e) & 1u) && lgv[e] > best; best = take ? lgv[e] : best; be = take ? e : be; }
;                     mask |= 1u << be; tv[k] = best; te[k] = be; }
	v_cmp_eq_u32_e64 s[10:11], 0, v28
	v_cmp_gt_f32_e64 s[12:13], v36, v18
	s_and_b64 s[10:11], s[10:11], s[12:13]
	v_cndmask_b32_e64 v18, v18, v36, s[10:11]
	v_and_b32_e32 v30, 4, v27
	v_cndmask_b32_e64 v28, 0, 1, s[10:11]
	v_cmp_eq_u32_e64 s[10:11], 0, v30
	v_cmp_gt_f32_e64 s[12:13], v14, v18
	s_and_b64 s[10:11], s[10:11], s[12:13]
	v_cndmask_b32_e64 v18, v18, v14, s[10:11]
	v_and_b32_e32 v30, 8, v27
	v_cndmask_b32_e64 v28, v28, 2, s[10:11]
	v_cmp_eq_u32_e64 s[10:11], 0, v30
	v_cmp_gt_f32_e64 s[12:13], v15, v18
	s_and_b64 s[10:11], s[10:11], s[12:13]
	v_cndmask_b32_e64 v18, v18, v15, s[10:11]
	v_and_b32_e32 v30, 16, v27
	v_cndmask_b32_e64 v28, v28, 3, s[10:11]
	v_cmp_eq_u32_e64 s[10:11], 0, v30
	v_cmp_gt_f32_e64 s[12:13], v39, v18
	s_and_b64 s[10:11], s[10:11], s[12:13]
	v_cndmask_b32_e64 v18, v18, v39, s[10:11]
	v_and_b32_e32 v30, 32, v27
	v_cndmask_b32_e64 v28, v28, 4, s[10:11]
	v_cmp_eq_u32_e64 s[10:11], 0, v30
	v_cmp_gt_f32_e64 s[12:13], v38, v18
	s_and_b64 s[10:11], s[10:11], s[12:13]
	v_cndmask_b32_e64 v18, v18, v38, s[10:11]
	v_and_b32_e32 v30, 64, v27
	v_cndmask_b32_e64 v28, v28, 5, s[10:11]
	v_cmp_eq_u32_e64 s[10:11], 0, v30
	v_cmp_gt_f32_e64 s[12:13], v10, v18
	s_and_b64 s[10:11], s[10:11], s[12:13]
	v_cndmask_b32_e64 v18, v18, v10, s[10:11]
	v_and_b32_e32 v30, 0x80, v27
	v_cndmask_b32_e64 v28, v28, 6, s[10:11]
	v_cmp_eq_u32_e64 s[10:11], 0, v30
	v_cmp_gt_f32_e64 s[12:13], v11, v18
	s_and_b64 s[10:11], s[10:11], s[12:13]
	v_cndmask_b32_e64 v18, v18, v11, s[10:11]
	v_and_b32_e32 v30, 0x100, v27
	v_cndmask_b32_e64 v28, v28, 7, s[10:11]
	v_cmp_eq_u32_e64 s[10:11], 0, v30
	v_cmp_gt_f32_e64 s[12:13], v41, v18
	s_and_b64 s[10:11], s[10:11], s[12:13]
	v_cndmask_b32_e64 v18, v18, v41, s[10:11]
	v_and_b32_e32 v30, 0x200, v27
	v_cndmask_b32_e64 v28, v28, 8, s[10:11]
	v_cmp_eq_u32_e64 s[10:11], 0, v30
	v_cmp_gt_f32_e64 s[12:13], v40, v18
	s_and_b64 s[10:11], s[10:11], s[12:13]
	v_cndmask_b32_e64 v18, v18, v40, s[10:11]
	v_and_b32_e32 v30, 0x400, v27
	v_cndmask_b32_e64 v28, v28, 9, s[10:11]
	v_cmp_eq_u32_e64 s[10:11], 0, v30
	v_cmp_gt_f32_e64 s[12:13], v6, v18
	s_and_b64 s[10:11], s[10:11], s[12:13]
	v_cndmask_b32_e64 v18, v18, v6, s[10:11]
	v_and_b32_e32 v30, 0x800, v27
	v_cndmask_b32_e64 v28, v28, 10, s[10:11]
	v_cmp_eq_u32_e64 s[10:11], 0, v30
	v_cmp_gt_f32_e64 s[12:13], v7, v18
	s_and_b64 s[10:11], s[10:11], s[12:13]
	v_cndmask_b32_e64 v18, v18, v7, s[10:11]
	v_and_b32_e32 v30, 0x1000, v27
	v_cndmask_b32_e64 v28, v28, 11, s[10:11]
	v_cmp_eq_u32_e64 s[10:11], 0, v30
	v_cmp_gt_f32_e64 s[12:13], v43, v18
	s_and_b64 s[10:11], s[10:11], s[12:13]
	v_cndmask_b32_e64 v18, v18, v43, s[10:11]
	v_and_b32_e32 v30, 0x2000, v27
	v_cndmask_b32_e64 v28, v28, 12, s[10:11]
	v_cmp_eq_u32_e64 s[10:11], 0, v30
	v_cmp_gt_f32_e64 s[12:13], v42, v18
	s_and_b64 s[10:11], s[10:11], s[12:13]
	v_cndmask_b32_e64 v18, v18, v42, s[10:11]
	v_and_b32_e32 v30, 0x4000, v27
	v_cndmask_b32_e64 v28, v28, 13, s[10:11]
	v_cmp_eq_u32_e64 s[10:11], 0, v30
	v_cmp_gt_f32_e64 s[12:13], v2, v18
	s_and_b64 s[10:11], s[10:11], s[12:13]
	v_cndmask_b32_e64 v18, v18, v2, s[10:11]
	v_and_b32_e32 v30, 0x8000, v27
	v_cndmask_b32_e64 v28, v28, 14, s[10:11]
	v_cmp_eq_u32_e64 s[10:11], 0, v30
	v_cmp_gt_f32_e64 s[12:13], v3, v18
	s_and_b64 s[10:11], s[10:11], s[12:13]
	v_cndmask_b32_e64 v18, v18, v3, s[10:11]
	v_and_b32_e32 v30, 0x10000, v27
	v_cndmask_b32_e64 v28, v28, 15, s[10:11]
	v_cmp_eq_u32_e64 s[10:11], 0, v30
	v_cmp_gt_f32_e64 s[12:13], v4, v18
	s_and_b64 s[10:11], s[10:11], s[12:13]
	v_cndmask_b32_e64 v18, v18, v4, s[10:11]
	v_and_b32_e32 v30, 0x20000, v27
	v_cndmask_b32_e64 v28, v28, 16, s[10:11]
	v_cmp_eq_u32_e64 s[10:11], 0, v30
	v_cmp_gt_f32_e64 s[12:13], v0, v18
	s_and_b64 s[10:11], s[10:11], s[12:13]
	v_cndmask_b32_e64 v18, v18, v0, s[10:11]
	v_and_b32_e32 v30, 0x40000, v27
	v_cndmask_b32_e64 v28, v28, 17, s[10:11]
	v_cmp_eq_u32_e64 s[10:11], 0, v30
	v_cmp_gt_f32_e64 s[12:13], v1, v18
	s_and_b64 s[10:11], s[10:11], s[12:13]
	v_cndmask_b32_e64 v18, v18, v1, s[10:11]
	v_and_b32_e32 v30, 0x80000, v27
	v_cndmask_b32_e64 v28, v28, 18, s[10:11]
	v_cmp_eq_u32_e64 s[10:11], 0, v30
	v_cmp_gt_f32_e64 s[12:13], v33, v18
	s_and_b64 s[10:11], s[10:11], s[12:13]
	v_cndmask_b32_e64 v18, v18, v33, s[10:11]
	v_and_b32_e32 v30, 0x100000, v27
	v_cndmask_b32_e64 v28, v28, 19, s[10:11]
	v_cmp_eq_u32_e64 s[10:11], 0, v30
	v_cmp_gt_f32_e64 s[12:13], v8, v18
	s_and_b64 s[10:11], s[10:11], s[12:13]
	v_cndmask_b32_e64 v18, v18, v8, s[10:11]
	v_and_b32_e32 v30, 0x200000, v27
	v_cndmask_b32_e64 v28, v28, 20, s[10:11]
	v_cmp_eq_u32_e64 s[10:11], 0, v30
	v_cmp_gt_f32_e64 s[12:13], v5, v18
	s_and_b64 s[10:11], s[10:11], s[12:13]
	v_cndmask_b32_e64 v18, v18, v5, s[10:11]
	v_and_b32_e32 v30, 0x400000, v27
	v_cndmask_b32_e64 v28, v28, 21, s[10:11]
	v_cmp_eq_u32_e64 s[10:11], 0, v30
	v_cmp_gt_f32_e64 s[12:13], v9, v18
	s_and_b64 s[10:11], s[10:11], s[12:13]
	v_cndmask_b32_e64 v18, v18, v9, s[10:11]
	v_and_b32_e32 v30, 0x800000, v27
	v_cndmask_b32_e64 v28, v28, 22, s[10:11]
	v_cmp_eq_u32_e64 s[10:11], 0, v30
	v_cmp_gt_f32_e64 s[12:13], v29, v18
	s_and_b64 s[10:11], s[10:11], s[12:13]
	v_cndmask_b32_e64 v18, v18, v29, s[10:11]
	v_and_b32_e32 v30, 0x1000000, v27
	v_cndmask_b32_e64 v28, v28, 23, s[10:11]
	v_cmp_eq_u32_e64 s[10:11], 0, v30
	v_cmp_gt_f32_e64 s[12:13], v13, v18
	s_and_b64 s[10:11], s[10:11], s[12:13]
	v_cndmask_b32_e64 v18, v18, v13, s[10:11]
	v_and_b32_e32 v30, 0x2000000, v27
	v_cndmask_b32_e64 v28, v28, 24, s[10:11]
	v_cmp_eq_u32_e64 s[10:11], 0, v30
	v_cmp_gt_f32_e64 s[12:13], v12, v18
	s_and_b64 s[10:11], s[10:11], s[12:13]
	v_cndmask_b32_e64 v18, v18, v12, s[10:11]
	v_and_b32_e32 v30, 0x4000000, v27
; __global__ void __launch_bounds__(512, 2) fwd_kernel(Params p) {
;     ...
;                 unsigned mask = 0u; float tv[4];
; #pragma unroll
;                 for (int k = 0; k < 4; ++k) { float best = -__builtin_inff(); int be = 0;
; #pragma unroll
;                     for (int e = 0; e < NE; ++e) { const bool take = !((mask >> e) & 1u) && lgv[e] > best; best = take ? lgv[e] : best; be = take ? e : be; }
;                     mask |= 1u << be; tv[k] = best; te[k] = be; }
	v_cndmask_b32_e64 v28, v28, 25, s[10:11]
	v_cmp_eq_u32_e64 s[10:11], 0, v30
	v_cmp_gt_f32_e64 s[12:13], v22, v18
	s_and_b64 s[10:11], s[10:11], s[12:13]
	v_cndmask_b32_e64 v18, v18, v22, s[10:11]
	v_and_b32_e32 v30, 0x8000000, v27
	v_cndmask_b32_e64 v28, v28, 26, s[10:11]
	v_cmp_eq_u32_e64 s[10:11], 0, v30
	v_cmp_gt_f32_e64 s[12:13], v25, v18
	s_and_b64 s[10:11], s[10:11], s[12:13]
	v_cndmask_b32_e64 v18, v18, v25, s[10:11]
	v_and_b32_e32 v30, 0x10000000, v27
	v_cndmask_b32_e64 v28, v28, 27, s[10:11]
	v_cmp_eq_u32_e64 s[10:11], 0, v30
	v_cmp_gt_f32_e64 s[12:13], v23, v18
	s_and_b64 s[10:11], s[10:11], s[12:13]
	v_cndmask_b32_e64 v18, v18, v23, s[10:11]
	v_and_b32_e32 v30, 0x20000000, v27
	v_cndmask_b32_e64 v28, v28, 28, s[10:11]
	v_cmp_eq_u32_e64 s[10:11], 0, v30
	v_cmp_gt_f32_e64 s[12:13], v19, v18
	s_and_b64 s[10:11], s[10:11], s[12:13]
	v_cndmask_b32_e64 v18, v18, v19, s[10:11]
	v_and_b32_e32 v30, 2.0, v27
	v_cndmask_b32_e64 v28, v28, 29, s[10:11]
	v_cmp_eq_u32_e64 s[10:11], 0, v30
	v_cmp_gt_f32_e64 s[12:13], v20, v18
	s_and_b64 s[10:11], s[10:11], s[12:13]
	v_cndmask_b32_e64 v30, v18, v20, s[10:11]
	v_cndmask_b32_e64 v28, v28, 30, s[10:11]
	v_cmp_lt_i32_e64 s[10:11], -1, v27
	v_cmp_gt_f32_e64 s[12:13], v21, v30
	s_and_b64 s[10:11], s[10:11], s[12:13]
	v_cndmask_b32_e64 v18, v28, 31, s[10:11]
	v_cndmask_b32_e64 v28, v30, v21, s[10:11]
	v_lshlrev_b32_e64 v30, v18, 1
	v_or_b32_e32 v31, v30, v27
	v_and_b32_e32 v32, 1, v31
	v_cmp_eq_u32_e64 s[10:11], 1, v32
	s_or_b64 vcc, s[10:11], vcc
	v_cndmask_b32_e32 v32, v37, v139, vcc
	v_bitop3_b32 v37, v30, 2, v27 bitop3:0xc8
	v_cmp_eq_u32_e32 vcc, 0, v37
	v_cmp_gt_f32_e64 s[10:11], v36, v32
	s_and_b64 vcc, vcc, s[10:11]
	v_cndmask_b32_e32 v32, v32, v36, vcc
	v_bitop3_b32 v36, v30, 4, v27 bitop3:0xc8
	v_cndmask_b32_e64 v37, 0, 1, vcc
	v_cmp_eq_u32_e32 vcc, 0, v36
	v_cmp_gt_f32_e64 s[10:11], v14, v32
	s_and_b64 vcc, vcc, s[10:11]
	v_cndmask_b32_e32 v14, v32, v14, vcc
	v_bitop3_b32 v32, v30, 8, v27 bitop3:0xc8
	v_cndmask_b32_e64 v36, v37, 2, vcc
	v_cmp_eq_u32_e32 vcc, 0, v32
	v_cmp_gt_f32_e64 s[10:11], v15, v14
	s_and_b64 vcc, vcc, s[10:11]
	v_cndmask_b32_e32 v14, v14, v15, vcc
	v_bitop3_b32 v15, v30, 16, v27 bitop3:0xc8
	v_cndmask_b32_e64 v32, v36, 3, vcc
	v_cmp_eq_u32_e32 vcc, 0, v15
	v_cmp_gt_f32_e64 s[10:11], v39, v14
	s_and_b64 vcc, vcc, s[10:11]
	v_cndmask_b32_e64 v15, v32, 4, vcc
	v_cndmask_b32_e32 v14, v14, v39, vcc
	v_bitop3_b32 v32, v30, 32, v27 bitop3:0xc8
	v_cmp_eq_u32_e32 vcc, 0, v32
	v_cmp_gt_f32_e64 s[10:11], v38, v14
	s_and_b64 vcc, vcc, s[10:11]
	v_cndmask_b32_e32 v14, v14, v38, vcc
	v_bitop3_b32 v32, v30, 64, v27 bitop3:0xc8
	v_cndmask_b32_e64 v15, v15, 5, vcc
	v_cmp_eq_u32_e32 vcc, 0, v32
	v_cmp_gt_f32_e64 s[10:11], v10, v14
	s_and_b64 vcc, vcc, s[10:11]
	v_cndmask_b32_e32 v10, v14, v10, vcc
	v_bitop3_b32 v14, v30, s0, v27 bitop3:0xc8
	v_cndmask_b32_e64 v15, v15, 6, vcc
	v_cmp_eq_u32_e32 vcc, 0, v14
	v_cmp_gt_f32_e64 s[10:11], v11, v10
	s_and_b64 vcc, vcc, s[10:11]
	s_movk_i32 s0, 0x100
	v_cndmask_b32_e32 v10, v10, v11, vcc
	v_bitop3_b32 v11, v30, s0, v27 bitop3:0xc8
	v_cndmask_b32_e64 v14, v15, 7, vcc
	v_cmp_eq_u32_e32 vcc, 0, v11
	v_cmp_gt_f32_e64 s[10:11], v41, v10
	s_and_b64 vcc, vcc, s[10:11]
	s_movk_i32 s0, 0x200
	v_cndmask_b32_e64 v11, v14, 8, vcc
	v_cndmask_b32_e32 v10, v10, v41, vcc
	v_bitop3_b32 v14, v30, s0, v27 bitop3:0xc8
	v_cmp_eq_u32_e32 vcc, 0, v14
	v_cmp_gt_f32_e64 s[10:11], v40, v10
	s_and_b64 vcc, vcc, s[10:11]
	s_movk_i32 s0, 0x400
	v_cndmask_b32_e32 v10, v10, v40, vcc
	v_bitop3_b32 v14, v30, s0, v27 bitop3:0xc8
	v_cndmask_b32_e64 v11, v11, 9, vcc
	v_cmp_eq_u32_e32 vcc, 0, v14
	v_cmp_gt_f32_e64 s[10:11], v6, v10
	s_and_b64 vcc, vcc, s[10:11]
	v_cndmask_b32_e32 v6, v10, v6, vcc
	v_bitop3_b32 v10, v30, s59, v27 bitop3:0xc8
	v_cndmask_b32_e64 v11, v11, 10, vcc
	v_cmp_eq_u32_e32 vcc, 0, v10
	v_cmp_gt_f32_e64 s[10:11], v7, v6
	s_and_b64 vcc, vcc, s[10:11]
	v_cndmask_b32_e32 v6, v6, v7, vcc
	v_bitop3_b32 v7, v30, s60, v27 bitop3:0xc8
	v_cndmask_b32_e64 v10, v11, 11, vcc
	v_cmp_eq_u32_e32 vcc, 0, v7
	v_cmp_gt_f32_e64 s[10:11], v43, v6
	s_and_b64 vcc, vcc, s[10:11]
	v_cndmask_b32_e64 v7, v10, 12, vcc
	v_cndmask_b32_e32 v6, v6, v43, vcc
	v_bitop3_b32 v10, v30, s61, v27 bitop3:0xc8
	v_cmp_eq_u32_e32 vcc, 0, v10
	v_cmp_gt_f32_e64 s[10:11], v42, v6
	s_and_b64 vcc, vcc, s[10:11]
	s_movk_i32 s0, 0x4000
	v_cndmask_b32_e32 v6, v6, v42, vcc
	v_bitop3_b32 v10, v30, s0, v27 bitop3:0xc8
	v_cndmask_b32_e64 v7, v7, 13, vcc
	v_cmp_eq_u32_e32 vcc, 0, v10
	v_cmp_gt_f32_e64 s[10:11], v2, v6
	s_and_b64 vcc, vcc, s[10:11]
	v_cndmask_b32_e32 v2, v6, v2, vcc
	v_bitop3_b32 v6, v30, s62, v27 bitop3:0xc8
	v_cndmask_b32_e64 v7, v7, 14, vcc
	v_cmp_eq_u32_e32 vcc, 0, v6
	v_cmp_gt_f32_e64 s[10:11], v3, v2
	s_and_b64 vcc, vcc, s[10:11]
	v_cndmask_b32_e32 v2, v2, v3, vcc
	v_bitop3_b32 v3, v30, s63, v27 bitop3:0xc8
	v_cndmask_b32_e64 v6, v7, 15, vcc
	v_cmp_eq_u32_e32 vcc, 0, v3
	v_cmp_gt_f32_e64 s[10:11], v4, v2
	s_and_b64 vcc, vcc, s[10:11]
	v_cndmask_b32_e32 v2, v2, v4, vcc
; __global__ void __launch_bounds__(512, 2) fwd_kernel(Params p) {
;     ...
;                 for (int k = 0; k < 4; ++k) { float best = -__builtin_inff(); int be = 0;
; #pragma unroll
;                     for (int e = 0; e < NE; ++e) { const bool take = !((mask >> e) & 1u) && lgv[e] > best; best = take ? lgv[e] : best; be = take ? e : be; }
;                     mask |= 1u << be; tv[k] = best; te[k] = be; }
;                 float ex[4], sum = 0.f;
; #pragma unroll
;                 for (int k = 0; k < 4; ++k) { ex[k] = __expf(tv[k] - tv[0]); sum += ex[k]; }
;                 const float inv = 1.0f / sum;
; #pragma unroll
;                 for (int k = 0; k < 4; ++k) { lrk[tid * 4 + k] = atomicAdd((int*)&hist[te[k]], 1); tok_e[tok * 4 + k] = te[k]; tok_w[tok * 4 + k] = ex[k] * inv; }
	v_bitop3_b32 v4, v30, s64, v27 bitop3:0xc8
	v_cndmask_b32_e64 v3, v6, 16, vcc
	v_cmp_eq_u32_e32 vcc, 0, v4
	v_cmp_gt_f32_e64 s[10:11], v0, v2
	s_and_b64 vcc, vcc, s[10:11]
	v_cndmask_b32_e32 v0, v2, v0, vcc
	v_bitop3_b32 v2, v30, s65, v27 bitop3:0xc8
	v_cndmask_b32_e64 v3, v3, 17, vcc
	v_cmp_eq_u32_e32 vcc, 0, v2
	v_cmp_gt_f32_e64 s[10:11], v1, v0
	s_and_b64 vcc, vcc, s[10:11]
	v_cndmask_b32_e32 v0, v0, v1, vcc
	v_bitop3_b32 v1, v30, s66, v27 bitop3:0xc8
	v_cndmask_b32_e64 v2, v3, 18, vcc
	v_cmp_eq_u32_e32 vcc, 0, v1
	v_cmp_gt_f32_e64 s[10:11], v33, v0
	s_and_b64 vcc, vcc, s[10:11]
	v_cndmask_b32_e64 v1, v2, 19, vcc
	v_cndmask_b32_e32 v0, v0, v33, vcc
	v_bitop3_b32 v2, v30, s67, v27 bitop3:0xc8
	v_cmp_eq_u32_e32 vcc, 0, v2
	v_cmp_gt_f32_e64 s[10:11], v8, v0
	s_and_b64 vcc, vcc, s[10:11]
	v_cndmask_b32_e32 v0, v0, v8, vcc
	v_bitop3_b32 v2, v30, s68, v27 bitop3:0xc8
	v_cndmask_b32_e64 v1, v1, 20, vcc
	v_cmp_eq_u32_e32 vcc, 0, v2
	v_cmp_gt_f32_e64 s[10:11], v5, v0
	s_and_b64 vcc, vcc, s[10:11]
	v_cndmask_b32_e32 v0, v0, v5, vcc
	v_bitop3_b32 v2, v30, s69, v27 bitop3:0xc8
	v_cndmask_b32_e64 v1, v1, 21, vcc
	v_cmp_eq_u32_e32 vcc, 0, v2
	v_cmp_gt_f32_e64 s[10:11], v9, v0
	s_and_b64 vcc, vcc, s[10:11]
	v_cndmask_b32_e32 v0, v0, v9, vcc
	v_bitop3_b32 v2, v30, s57, v27 bitop3:0xc8
	v_cndmask_b32_e64 v1, v1, 22, vcc
	v_cmp_eq_u32_e32 vcc, 0, v2
	v_cmp_gt_f32_e64 s[10:11], v29, v0
	s_and_b64 vcc, vcc, s[10:11]
	v_cndmask_b32_e32 v0, v0, v29, vcc
	v_bitop3_b32 v2, v30, s70, v27 bitop3:0xc8
	v_cndmask_b32_e64 v1, v1, 23, vcc
	v_cmp_eq_u32_e32 vcc, 0, v2
	v_cmp_gt_f32_e64 s[10:11], v13, v0
	s_and_b64 vcc, vcc, s[10:11]
	v_cndmask_b32_e32 v0, v0, v13, vcc
	v_bitop3_b32 v2, v30, s71, v27 bitop3:0xc8
	v_cndmask_b32_e64 v1, v1, 24, vcc
	v_cmp_eq_u32_e32 vcc, 0, v2
	v_cmp_gt_f32_e64 s[10:11], v12, v0
	s_and_b64 vcc, vcc, s[10:11]
	v_cndmask_b32_e32 v0, v0, v12, vcc
	v_bitop3_b32 v2, v30, s72, v27 bitop3:0xc8
	v_cndmask_b32_e64 v1, v1, 25, vcc
	v_cmp_eq_u32_e32 vcc, 0, v2
	v_cmp_gt_f32_e64 s[10:11], v22, v0
	s_and_b64 vcc, vcc, s[10:11]
	v_cndmask_b32_e32 v0, v0, v22, vcc
	v_bitop3_b32 v2, v30, s73, v27 bitop3:0xc8
	v_cndmask_b32_e64 v1, v1, 26, vcc
	v_cmp_eq_u32_e32 vcc, 0, v2
	v_cmp_gt_f32_e64 s[10:11], v25, v0
	s_and_b64 vcc, vcc, s[10:11]
	v_cndmask_b32_e32 v0, v0, v25, vcc
	v_bitop3_b32 v2, v30, s74, v27 bitop3:0xc8
	v_cndmask_b32_e64 v1, v1, 27, vcc
	v_cmp_eq_u32_e32 vcc, 0, v2
	v_cmp_gt_f32_e64 s[10:11], v23, v0
	s_and_b64 vcc, vcc, s[10:11]
	v_cndmask_b32_e32 v0, v0, v23, vcc
	v_bitop3_b32 v2, v30, s75, v27 bitop3:0xc8
	v_cndmask_b32_e64 v1, v1, 28, vcc
	v_cmp_eq_u32_e32 vcc, 0, v2
	v_cmp_gt_f32_e64 s[10:11], v19, v0
	s_and_b64 vcc, vcc, s[10:11]
	v_cndmask_b32_e32 v0, v0, v19, vcc
	v_bitop3_b32 v2, v30, 2.0, v27 bitop3:0xc8
	v_cndmask_b32_e64 v1, v1, 29, vcc
	v_cmp_eq_u32_e32 vcc, 0, v2
	v_cmp_gt_f32_e64 s[10:11], v20, v0
	s_and_b64 vcc, vcc, s[10:11]
	v_cndmask_b32_e32 v0, v0, v20, vcc
	v_cndmask_b32_e64 v1, v1, 30, vcc
	v_cmp_lt_i32_e32 vcc, -1, v31
	v_cmp_gt_f32_e64 s[10:11], v21, v0
	s_and_b64 vcc, vcc, s[10:11]
	v_cndmask_b32_e64 v19, v1, 31, vcc
	v_sub_f32_e32 v1, v24, v24
	v_sub_f32_e32 v2, v26, v24
	v_mul_f32_e32 v1, 0x3fb8aa3b, v1
	v_mul_f32_e32 v2, 0x3fb8aa3b, v2
	v_cndmask_b32_e32 v0, v0, v21, vcc
	v_exp_f32_e32 v6, v1
	v_exp_f32_e32 v7, v2
	v_sub_f32_e32 v2, v28, v24
	v_mul_f32_e32 v2, 0x3fb8aa3b, v2
	v_sub_f32_e32 v0, v0, v24
	v_exp_f32_e32 v8, v2
	v_mul_f32_e32 v0, 0x3fb8aa3b, v0
	v_exp_f32_e32 v9, v0
	v_add_f32_e32 v1, 0, v6
	v_add_f32_e32 v1, v1, v7
	v_add_f32_e32 v1, v1, v8
	v_add_f32_e32 v0, v1, v9
	v_div_scale_f32 v1, s[0:1], v0, v0, 1.0
	v_rcp_f32_e32 v2, v1
	v_add_u32_e32 v11, 0, v134
	v_fma_f32 v3, -v1, v2, 1.0
	v_fmac_f32_e32 v2, v3, v2
	v_div_scale_f32 v3, vcc, 1.0, v0, 1.0
	v_mul_f32_e32 v4, v3, v2
	v_fma_f32 v5, -v1, v4, v3
	v_fmac_f32_e32 v4, v5, v2
	v_fma_f32 v1, -v1, v4, v3
	v_div_fmas_f32 v1, v1, v2, v4
	v_div_fixup_f32 v10, v1, v0, 1.0
	v_lshl_add_u32 v1, v16, 2, 0
	ds_add_rtn_u32 v1, v1, v138 offset:53760
	v_lshlrev_b32_e32 v0, 2, v34
	s_waitcnt lgkmcnt(0)
	ds_write_b32 v11, v1 offset:40960
	v_ashrrev_i32_e32 v1, 31, v0
	v_lshlrev_b64 v[2:3], 2, v[0:1]
	v_lshl_add_u64 v[4:5], s[16:17], 0, v[2:3]
	v_mul_f32_e32 v1, v10, v6
	v_mov_b32_e32 v240, v1
	v_lshl_add_u64 v[2:3], s[42:43], 0, v[2:3]
	global_store_dword v[2:3], v1, off
	v_lshl_add_u32 v1, v17, 2, 0
	ds_add_rtn_u32 v1, v1, v138 offset:53760
	v_or_b32_e32 v2, 1, v0
	v_ashrrev_i32_e32 v3, 31, v2
	v_mul_f32_e32 v0, v10, v7
	v_lshl_add_u64 v[6:7], v[2:3], 2, s[42:43]
	s_waitcnt lgkmcnt(0)
	ds_write_b32 v11, v1 offset:40964
	v_lshl_add_u32 v1, v18, 2, 0
	ds_add_rtn_u32 v1, v1, v138 offset:53760
	v_lshl_add_u32 v2, v19, 2, 0
	s_waitcnt lgkmcnt(0)
	ds_write_b32 v11, v1 offset:40968
	ds_add_rtn_u32 v2, v2, v138 offset:53760
	v_mul_f32_e32 v1, v10, v8
	global_store_dwordx4 v[4:5], v[16:19], off
	s_waitcnt lgkmcnt(0)
	ds_write_b32 v11, v2 offset:40972
	v_mul_f32_e32 v2, v10, v9
	v_mov_b32_e32 v241, v0
	v_mov_b32_e32 v242, v1
	v_mov_b32_e32 v243, v2
	global_store_dwordx3 v[6:7], v[0:2], off
